# speedup vs baseline: 1.0190x; 1.0031x over previous
_Z10ode_kernelPKfPKDF16_S2_PfPKi:
	v_lshrrev_b32_e32 v167, 6, v0
	s_lshr_b32 s3, s2, 3
	v_add_u32_e32 v2, s3, v167
	s_load_dwordx4 s[4:7], s[0:1], 0x0
	s_load_dwordx2 s[12:13], s[0:1], 0x10
	v_and_b32_e32 v130, 3, v2
	v_and_b32_e32 v1, 63, v0
	v_readfirstlane_b32 s3, v130
	v_lshlrev_b32_e32 v166, 4, v1
	s_lshl_b32 s11, s3, 14
	v_lshl_or_b32 v2, v130, 17, v166
	v_mov_b32_e32 v3, 0
	s_and_b32 s17, s11, 0xc000
	s_mov_b32 s9, 0
	s_waitcnt lgkmcnt(0)
	v_lshl_add_u64 v[74:75], s[6:7], 0, v[2:3]
	s_lshl_b32 s8, s17, 1
	v_lshl_add_u64 v[46:47], v[74:75], 0, s[8:9]
	s_movk_i32 s15, 0x1000
	v_add_co_u32_e32 v18, vcc, s15, v46
	s_movk_i32 s14, 0x3000
	s_nop 0
	v_addc_co_u32_e32 v19, vcc, 0, v47, vcc
	v_add_co_u32_e32 v20, vcc, s14, v46
	s_lshl_b32 s10, s2, 10
	s_nop 0
	v_addc_co_u32_e32 v21, vcc, 0, v47, vcc
	s_and_b32 s8, s10, 0x3e000
	s_movk_i32 s16, 0x7000
	v_add_co_u32_e32 v48, vcc, s16, v46
	v_lshl_or_b32 v22, v1, 7, s8
	s_add_i32 s8, s11, 0x4000
	v_addc_co_u32_e32 v49, vcc, 0, v47, vcc
	s_movk_i32 s16, 0x5000
	s_and_b32 s8, s8, 0xc000
	v_add_co_u32_e32 v50, vcc, s16, v46
	s_lshl_b32 s8, s8, 1
	global_load_dwordx4 v[34:37], v[18:19], off offset:2048
	global_load_dwordx4 v[14:17], v[20:21], off offset:2048
	global_load_dwordx4 v[6:9], v[20:21], off offset:1024
	global_load_dwordx4 v[2:5], v[18:19], off offset:1024
	global_load_dwordx4 v[42:45], v[18:19], off offset:3072
	global_load_dwordx4 v[38:41], v[20:21], off offset:3072
	v_addc_co_u32_e32 v51, vcc, 0, v47, vcc
	v_lshl_add_u64 v[72:73], v[74:75], 0, s[8:9]
	v_add_co_u32_e32 v106, vcc, s14, v72
	global_load_dwordx4 v[10:13], v[50:51], off offset:1024
	global_load_dwordx4 v[52:55], v[50:51], off offset:2048
	global_load_dwordx4 v[56:59], v[48:49], off offset:2048
	v_addc_co_u32_e32 v107, vcc, 0, v73, vcc
	v_add_co_u32_e32 v108, vcc, s15, v72
	global_load_dwordx4 v[60:63], v[50:51], off offset:3072
	global_load_dwordx4 v[64:67], v[48:49], off offset:3072
	global_load_ushort v198, v22, s[12:13]
	v_addc_co_u32_e32 v109, vcc, 0, v73, vcc
	global_load_dwordx4 v[68:71], v[108:109], off offset:2048
	global_load_dwordx4 v[78:81], v[106:107], off offset:2048
	global_load_dwordx4 v[82:85], v[106:107], off offset:3072
	global_load_dwordx4 v[86:89], v[108:109], off offset:3072
	s_add_i32 s8, s11, 0x6000
	s_movk_i32 s16, 0x2000
	s_and_b32 s8, s8, 0xe000
	v_add_co_u32_e32 v26, vcc, s16, v46
	s_lshl_b32 s8, s8, 1
	s_nop 0
	v_addc_co_u32_e32 v27, vcc, 0, v47, vcc
	v_lshl_add_u64 v[110:111], v[74:75], 0, s[8:9]
	v_add_co_u32_e32 v112, vcc, s14, v110
	global_load_dwordx4 a[0:3], v[46:47], off
	global_load_dwordx4 a[8:11], v[46:47], off offset:1024
	global_load_dwordx4 a[12:15], v[26:27], off offset:1024
	global_load_dwordx4 a[20:23], v[26:27], off offset:2048
	global_load_dwordx4 a[16:19], v[46:47], off offset:2048
	global_load_dwordx4 a[24:27], v[46:47], off offset:3072
	global_load_dwordx4 a[4:7], v[20:21], off offset:-4096
	global_load_dwordx4 v[22:25], v[20:21], off
	global_load_dwordx4 a[28:31], v[26:27], off offset:3072
	s_nop 0
	global_load_dwordx4 v[18:21], v[18:19], off
	v_addc_co_u32_e32 v113, vcc, 0, v111, vcc
	v_add_co_u32_e32 v114, vcc, s15, v110
	v_lshl_or_b32 v199, v167, 15, v166
	s_nop 0
	v_addc_co_u32_e32 v115, vcc, 0, v111, vcc
	global_load_dwordx4 v[26:29], v[114:115], off offset:1024
	global_load_dwordx4 v[90:93], v[114:115], off offset:2048
	global_load_dwordx4 v[30:33], v[112:113], off offset:1024
	global_load_dwordx4 v[94:97], v[112:113], off offset:2048
	global_load_dwordx4 v[98:101], v[114:115], off offset:3072
	global_load_dwordx4 v[102:105], v[112:113], off offset:3072
	s_movk_i32 s8, 0x6000
	s_load_dwordx2 s[6:7], s[0:1], 0x20
	v_lshlrev_b32_e32 v76, 1, v0
	v_and_b32_e32 v200, 7, v0
	v_and_b32_e32 v128, 64, v76
	v_and_b32_e32 v179, 15, v0
	v_bfe_u32 v201, v0, 4, 1
	v_mov_b32_e32 v196, 0x44444444
	global_load_dwordx4 a[44:47], v[48:49], off offset:-4096
	s_waitcnt vmcnt(31)
	ds_write_b128 v199, v[14:17] offset:1024
	v_add_co_u32_e32 v14, vcc, s8, v46
	s_movk_i32 s8, 0x4000
	s_nop 0
	v_addc_co_u32_e32 v15, vcc, 0, v47, vcc
	s_waitcnt vmcnt(28)
	ds_write_b128 v199, v[42:45] offset:2048
	v_add_co_u32_e32 v42, vcc, s8, v46
	ds_write_b128 v199, v[34:37]
	s_nop 0
	v_addc_co_u32_e32 v43, vcc, 0, v47, vcc
	s_waitcnt vmcnt(27)
	ds_write_b128 v199, v[38:41] offset:3072
	v_add_co_u32_e32 v44, vcc, s16, v72
	global_load_dwordx4 a[36:39], v[14:15], off offset:1024
	global_load_dwordx4 a[32:35], v[42:43], off offset:1024
	global_load_dwordx4 a[48:51], v[42:43], off offset:2048
	global_load_dwordx4 a[52:55], v[14:15], off offset:2048
	global_load_dwordx4 a[60:63], v[14:15], off offset:3072
	global_load_dwordx4 a[40:43], v[50:51], off offset:-4096
	global_load_dwordx4 v[34:37], v[50:51], off
	global_load_dwordx4 v[38:41], v[48:49], off
	s_nop 0
	global_load_dwordx4 v[14:17], v[48:49], off offset:1024
	s_waitcnt vmcnt(34)
	ds_write_b128 v199, v[52:55] offset:4096
	s_waitcnt vmcnt(33)
	ds_write_b128 v199, v[56:59] offset:5120
	v_addc_co_u32_e32 v45, vcc, 0, v73, vcc
	s_xor_b32 s8, s17, 0x8000
	global_load_dwordx4 a[68:71], v[106:107], off offset:-4096
	s_waitcnt vmcnt(33)
	ds_write_b128 v199, v[60:63] offset:6144
	s_waitcnt vmcnt(32)
	ds_write_b128 v199, v[64:67] offset:7168
	v_add_co_u32_e32 v58, vcc, s16, v110
	s_lshl_b32 s8, s8, 1
	global_load_dwordx4 a[56:59], v[42:43], off offset:3072
	global_load_dwordx4 a[64:67], v[72:73], off
	global_load_dwordx4 a[72:75], v[72:73], off offset:1024
	global_load_dwordx4 a[80:83], v[72:73], off offset:2048
	global_load_dwordx4 a[84:87], v[44:45], off offset:2048
	global_load_dwordx4 a[92:95], v[44:45], off offset:3072
	global_load_dwordx4 a[76:79], v[44:45], off offset:1024
	global_load_dwordx4 a[88:91], v[72:73], off offset:3072
	global_load_dwordx4 v[46:49], v[106:107], off
	global_load_dwordx4 v[54:57], v[106:107], off offset:1024
	s_nop 0
	global_load_dwordx4 v[42:45], v[108:109], off
	global_load_dwordx4 v[50:53], v[108:109], off offset:1024
	s_waitcnt vmcnt(42)
	ds_write_b128 v199, v[68:71] offset:8192
	s_waitcnt vmcnt(41)
	ds_write_b128 v199, v[78:81] offset:9216
	s_waitcnt vmcnt(39)
	ds_write_b128 v199, v[86:89] offset:10240
	ds_write_b128 v199, v[82:85] offset:11264
	v_addc_co_u32_e32 v59, vcc, 0, v111, vcc
	v_lshl_add_u64 v[78:79], v[74:75], 0, s[8:9]
	v_add_co_u32_e32 v84, vcc, s14, v78
	global_load_dwordx4 a[96:99], v[110:111], off
	global_load_dwordx4 a[104:107], v[110:111], off offset:1024
	global_load_dwordx4 a[108:111], v[58:59], off offset:1024
	global_load_dwordx4 a[116:119], v[58:59], off offset:2048
	global_load_dwordx4 a[112:115], v[110:111], off offset:2048
	global_load_dwordx4 a[120:123], v[110:111], off offset:3072
	global_load_dwordx4 a[100:103], v[112:113], off offset:-4096
	global_load_dwordx4 v[62:65], v[112:113], off
	global_load_dwordx4 a[124:127], v[58:59], off offset:3072
	s_nop 0
	global_load_dwordx4 v[58:61], v[114:115], off
	v_addc_co_u32_e32 v85, vcc, 0, v79, vcc
	v_add_co_u32_e32 v82, vcc, s15, v78
	s_add_i32 s8, s11, 0xa000
	s_nop 0
	v_addc_co_u32_e32 v83, vcc, 0, v79, vcc
	global_load_dwordx4 v[110:113], v[82:83], off offset:2048
	global_load_dwordx4 v[106:109], v[84:85], off offset:2048
	s_waitcnt vmcnt(39)
	ds_write_b128 v199, v[90:93] offset:12288
	s_waitcnt vmcnt(37)
	ds_write_b128 v199, v[94:97] offset:13312
	s_waitcnt vmcnt(36)
	ds_write_b128 v199, v[98:101] offset:14336
	s_waitcnt vmcnt(35)
	ds_write_b128 v199, v[102:105] offset:15360
	global_load_dwordx4 a[128:131], v[78:79], off
	global_load_dwordx4 a[132:135], v[84:85], off offset:-4096
	global_load_dwordx4 a[136:139], v[78:79], off offset:1024
	global_load_dwordx4 a[144:147], v[78:79], off offset:2048
	global_load_dwordx4 v[102:105], v[82:83], off offset:3072
	global_load_dwordx4 v[98:101], v[84:85], off offset:3072
	s_and_b32 s8, s8, 0xe000
	v_add_co_u32_e32 v80, vcc, s16, v78
	s_lshl_b32 s8, s8, 1
	s_nop 0
	v_addc_co_u32_e32 v81, vcc, 0, v79, vcc
	v_lshl_add_u64 v[122:123], v[74:75], 0, s[8:9]
	v_add_co_u32_e32 v124, vcc, s14, v122
	s_add_i32 s8, s11, 0xc000
	s_nop 0
	v_addc_co_u32_e32 v125, vcc, 0, v123, vcc
	v_add_co_u32_e32 v126, vcc, s15, v122
	s_and_b32 s8, s8, 0xc000
	s_nop 0
	v_addc_co_u32_e32 v127, vcc, 0, v123, vcc
	global_load_dwordx4 v[70:73], v[124:125], off offset:1024
	global_load_dwordx4 v[114:117], v[124:125], off offset:2048
	global_load_dwordx4 v[66:69], v[126:127], off offset:1024
	global_load_dwordx4 v[118:121], v[126:127], off offset:2048
	global_load_dwordx4 a[148:151], v[80:81], off offset:2048
	global_load_dwordx4 a[156:159], v[80:81], off offset:3072
	global_load_dwordx4 v[132:135], v[126:127], off offset:3072
	global_load_dwordx4 v[136:139], v[124:125], off offset:3072
	global_load_dwordx4 a[140:143], v[80:81], off offset:1024
	global_load_dwordx4 a[152:155], v[78:79], off offset:3072
	s_nop 0
	global_load_dwordx4 v[78:81], v[84:85], off
	global_load_dwordx4 v[86:89], v[84:85], off offset:1024
	s_lshl_b32 s8, s8, 1
	v_lshl_add_u64 v[164:165], v[74:75], 0, s[8:9]
	v_add_co_u32_e32 v176, vcc, s14, v164
	s_add_i32 s11, s11, 0xe000
	s_nop 0
	v_addc_co_u32_e32 v177, vcc, 0, v165, vcc
	v_add_co_u32_e32 v184, vcc, s15, v164
	s_and_b32 s8, s11, 0xe000
	s_nop 0
	v_addc_co_u32_e32 v185, vcc, 0, v165, vcc
	global_load_dwordx4 v[140:143], v[184:185], off offset:2048
	global_load_dwordx4 v[144:147], v[176:177], off offset:2048
	global_load_dwordx4 v[148:151], v[176:177], off offset:3072
	global_load_dwordx4 v[152:155], v[184:185], off offset:3072
	s_lshl_b32 s8, s8, 1
	v_lshl_add_u64 v[186:187], v[74:75], 0, s[8:9]
	v_add_co_u32_e32 v188, vcc, s14, v186
	v_and_or_b32 v74, v76, 16, v200
	s_nop 0
	v_addc_co_u32_e32 v189, vcc, 0, v187, vcc
	v_add_co_u32_e32 v190, vcc, s15, v186
	v_lshlrev_b32_e32 v129, 2, v74
	s_nop 0
	v_addc_co_u32_e32 v191, vcc, 0, v187, vcc
	global_load_dwordx4 v[94:97], v[188:189], off offset:1024
	global_load_dwordx4 v[156:159], v[188:189], off offset:2048
	global_load_dwordx4 v[90:93], v[190:191], off offset:1024
	global_load_dwordx4 v[160:163], v[190:191], off offset:2048
	global_load_dwordx4 v[172:175], v[188:189], off offset:3072
	global_load_dwordx4 v[180:183], v[190:191], off offset:3072
	s_waitcnt lgkmcnt(0)
	global_load_dword v131, v129, s[6:7]
	global_load_dwordx4 v[74:77], v[82:83], off
	s_nop 0
	global_load_dwordx4 v[82:85], v[82:83], off offset:1024
	s_waitcnt vmcnt(32)
	ds_write_b128 v199, v[110:113] offset:16384
	s_waitcnt vmcnt(31)
	ds_write_b128 v199, v[106:109] offset:17408
	v_lshlrev_b32_e32 v106, 7, v130
	v_or3_b32 v202, v106, v128, v179
	v_lshlrev_b32_e32 v106, 9, v201
	v_or_b32_e32 v107, 32, v129
	v_or3_b32 v106, v106, s10, v202
	global_load_dword v178, v129, s[6:7] offset:128
	global_load_dword v192, v107, s[6:7] offset:128
	global_load_dword v193, v129, s[6:7] offset:32
	v_ashrrev_i32_e32 v107, 31, v106
	v_lshl_add_u64 v[128:129], v[106:107], 2, s[4:5]
	global_load_dword v171, v[128:129], off
	s_waitcnt vmcnt(30)
	ds_write_b128 v199, v[102:105] offset:18432
	s_waitcnt vmcnt(29)
	ds_write_b128 v199, v[98:101] offset:19456
	v_add_co_u32_e32 v98, vcc, s16, v122
	s_mov_b32 s14, 0x45000000
	s_nop 0
	v_addc_co_u32_e32 v99, vcc, 0, v123, vcc
	global_load_dwordx4 a[160:163], v[122:123], off
	global_load_dwordx4 a[168:171], v[122:123], off offset:1024
	global_load_dwordx4 a[172:175], v[98:99], off offset:1024
	global_load_dwordx4 a[180:183], v[98:99], off offset:2048
	global_load_dwordx4 a[176:179], v[122:123], off offset:2048
	global_load_dwordx4 a[184:187], v[122:123], off offset:3072
	global_load_dword v170, v[128:129], off offset:64
	global_load_dwordx4 a[164:167], v[124:125], off offset:-4096
	global_load_dwordx4 v[102:105], v[124:125], off
	global_load_dwordx4 a[188:191], v[98:99], off offset:3072
	s_nop 0
	global_load_dwordx4 v[98:101], v[126:127], off
	s_waitcnt vmcnt(36)
	ds_write_b128 v199, v[118:121] offset:20480
	ds_write_b128 v199, v[114:117] offset:21504
	global_load_dword v169, v[128:129], off offset:128
	v_add_co_u32_e32 v106, vcc, s16, v164
	s_waitcnt vmcnt(34)
	ds_write_b128 v199, v[132:135] offset:22528
	s_waitcnt vmcnt(33)
	ds_write_b128 v199, v[136:139] offset:23552
	v_addc_co_u32_e32 v107, vcc, 0, v165, vcc
	global_load_dwordx4 a[192:195], v[164:165], off
	global_load_dwordx4 a[196:199], v[176:177], off offset:-4096
	global_load_dwordx4 a[200:203], v[164:165], off offset:1024
	global_load_dwordx4 a[208:211], v[164:165], off offset:2048
	global_load_dwordx4 a[212:215], v[106:107], off offset:2048
	global_load_dwordx4 a[220:223], v[106:107], off offset:3072
	global_load_dwordx4 a[204:207], v[106:107], off offset:1024
	global_load_dwordx4 a[216:219], v[164:165], off offset:3072
	global_load_dwordx4 v[110:113], v[176:177], off
	global_load_dwordx4 v[118:121], v[176:177], off offset:1024
	s_nop 0
	global_load_dwordx4 v[106:109], v[184:185], off
	global_load_dwordx4 v[114:117], v[184:185], off offset:1024
	global_load_dword v168, v[128:129], off offset:192
	v_add_co_u32_e32 v122, vcc, s16, v186
	v_and_b32_e32 v133, 32, v0
	s_nop 0
	v_addc_co_u32_e32 v123, vcc, 0, v187, vcc
	s_waitcnt vmcnt(41)
	ds_write_b128 v199, v[140:143] offset:24576
	s_waitcnt vmcnt(40)
	ds_write_b128 v199, v[144:147] offset:25600
	s_waitcnt vmcnt(38)
	ds_write_b128 v199, v[152:155] offset:26624
	ds_write_b128 v199, v[148:151] offset:27648
	global_load_dwordx4 a[224:227], v[186:187], off
	global_load_dwordx4 a[232:235], v[186:187], off offset:1024
	global_load_dwordx4 a[236:239], v[122:123], off offset:1024
	global_load_dwordx4 a[244:247], v[122:123], off offset:2048
	global_load_dwordx4 a[240:243], v[186:187], off offset:2048
	global_load_dwordx4 a[248:251], v[186:187], off offset:3072
	global_load_dwordx4 a[228:231], v[188:189], off offset:-4096
	global_load_dwordx4 v[126:129], v[188:189], off
	global_load_dwordx4 a[252:255], v[122:123], off offset:3072
	s_nop 0
	global_load_dwordx4 v[122:125], v[190:191], off
	v_lshlrev_b32_e32 v132, 2, v201
	v_lshl_or_b32 v130, v130, 6, v133
	v_lshrrev_b32_e32 v139, 1, v0
	v_and_b32_e32 v203, 24, v139
	s_waitcnt vmcnt(44)
	ds_write_b128 v199, v[160:163] offset:28672
	ds_write_b128 v199, v[156:159] offset:29696
	s_waitcnt vmcnt(42)
	ds_write_b128 v199, v[180:183] offset:30720
	ds_write_b128 v199, v[172:175] offset:31744
	s_waitcnt vmcnt(10) lgkmcnt(0)
	v_lshrrev_b32_e32 v222, 2, v131
	v_and_or_b32 v222, v222, 8, v132
	v_mul_u32_u24_e32 v222, 0x110, v222
	v_and_or_b32 v223, v131, 31, v130
	v_add_lshl_u32 v223, v223, v222, 1
	v_or_b32_e32 v204, 0x20000, v223
	v_lshrrev_b32_e32 v222, 2, v178
	v_and_or_b32 v222, v222, 8, v132
	v_mul_u32_u24_e32 v222, 0x110, v222
	v_and_or_b32 v223, v178, 31, v130
	v_add_lshl_u32 v223, v223, v222, 1
	v_or_b32_e32 v205, 0x20000, v223
	v_lshrrev_b32_e32 v222, 2, v193
	v_and_or_b32 v222, v222, 8, v132
	v_mul_u32_u24_e32 v222, 0x110, v222
	v_and_or_b32 v223, v193, 31, v130
	v_add_lshl_u32 v223, v223, v222, 1
	v_or_b32_e32 v206, 0x20000, v223
	v_lshrrev_b32_e32 v222, 2, v192
	v_and_or_b32 v222, v222, 8, v132
	v_mul_u32_u24_e32 v222, 0x110, v222
	v_and_or_b32 v223, v192, 31, v130
	v_add_lshl_u32 v223, v223, v222, 1
	v_or_b32_e32 v207, 0x20000, v223
	s_movk_i32 s43, 0x110
	v_mad_u32_u24 v224, v179, s43, v203
	v_mov_b32_e32 v225, 0x20000
	v_lshl_or_b32 v224, v224, 1, v225
	s_lshl_b32 s43, s3, 1
	s_add_u32 s52, s43, 0
	s_and_b32 s52, s52, 7
	s_lshl_b32 s52, s52, 6
	s_nop 0
	v_add_u32_e32 v208, s52, v224
	s_add_u32 s52, s43, 1
	s_and_b32 s52, s52, 7
	s_lshl_b32 s52, s52, 6
	s_sub_u32 s52, s52, 64
	s_nop 0
	v_add_u32_e32 v209, s52, v224
	s_add_u32 s52, s43, 2
	s_and_b32 s52, s52, 7
	s_lshl_b32 s52, s52, 6
	s_nop 0
	v_add_u32_e32 v211, s52, v224
	s_add_u32 s52, s43, 3
	s_and_b32 s52, s52, 7
	s_lshl_b32 s52, s52, 6
	s_nop 0
	v_add_u32_e32 v212, s52, v224
	s_add_u32 s52, s43, 4
	s_and_b32 s52, s52, 7
	s_lshl_b32 s52, s52, 6
	s_nop 0
	v_add_u32_e32 v213, s52, v224
	s_add_u32 s52, s43, 5
	s_and_b32 s52, s52, 7
	s_lshl_b32 s52, s52, 6
	s_nop 0
	v_add_u32_e32 v214, s52, v224
	s_add_u32 s52, s43, 6
	s_and_b32 s52, s52, 7
	s_lshl_b32 s52, s52, 6
	s_nop 0
	v_add_u32_e32 v215, s52, v224
	s_add_u32 s52, s43, 7
	s_and_b32 s52, s52, 7
	s_lshl_b32 s52, s52, 6
	s_nop 0
	v_add_u32_e32 v216, s52, v224
	v_and_b32_e32 v225, 8, v0
	v_cmp_eq_u32_e32 vcc, 0, v225
	v_mov_b32_e32 v225, 0xeeeeeeee
	s_nop 1
	v_cndmask_b32_e32 v210, v225, v196, vcc
	v_and_b32_e32 v225, 47, v0
	v_cmp_eq_u32_e64 s[4:5], 0, v225
	v_lshlrev_b32_e32 v225, 4, v167
	v_lshlrev_b32_e32 v226, 3, v201
	s_mov_b32 s52, 0x24400
	v_or3_b32 v218, v225, v226, s52
	s_load_dwordx2 s[6:7], s[0:1], 0x18
	s_lshl_b32 s11, s2, 9
	s_mov_b64 s[22:23], 0
	s_mov_b32 s29, 0
	s_mov_b32 s30, 0
	v_mov_b32_e32 v221, 0
	s_mov_b32 s40, 0x3a000000
	s_mov_b32 s41, 0x34800000
	s_mov_b32 s42, 0x45000000
	v_mov_b32_e32 v217, 0x24480
	v_mov_b64_e32 v[230:231], 0
	v_mov_b64_e32 v[232:233], 0
	v_mov_b64_e32 v[234:235], 0
	v_mov_b64_e32 v[236:237], 0
	v_mov_b64_e32 v[238:239], 0
	v_mov_b64_e32 v[240:241], 0
	v_mov_b64_e32 v[242:243], 0
	v_mov_b64_e32 v[244:245], 0
	ds_write_b128 v217, v[230:233]
	v_mov_b32_e32 v178, 0
	v_fma_mixlo_f16 v131, v178, v238, v171
	v_fma_mixlo_f16 v139, v178, v238, v170
	v_fma_mixlo_f16 v147, v178, v238, v169
	v_fma_mixlo_f16 v155, v178, v238, v168
	v_fma_f32 v130, v178, v238, v171
	v_fma_f32 v138, v178, v238, v170
	v_fma_f32 v146, v178, v238, v169
	v_fma_f32 v154, v178, v238, v168
	v_fma_mix_f32 v130, v130, 1.0, -v131 op_sel_hi:[0,0,1]
	v_fma_mix_f32 v138, v138, 1.0, -v139 op_sel_hi:[0,0,1]
	v_fma_mix_f32 v146, v146, 1.0, -v147 op_sel_hi:[0,0,1]
	v_fma_mix_f32 v154, v154, 1.0, -v155 op_sel_hi:[0,0,1]
	v_fma_mixlo_f16 v133, v130, s42, 0
	v_fma_mixlo_f16 v141, v138, s42, 0
	v_fma_mixlo_f16 v149, v146, s42, 0
	v_fma_mixlo_f16 v157, v154, s42, 0
	v_fma_mix_f32 v130, v130, s42, -v133 op_sel_hi:[0,0,1]
	v_fma_mix_f32 v138, v138, s42, -v141 op_sel_hi:[0,0,1]
	v_fma_mix_f32 v146, v146, s42, -v149 op_sel_hi:[0,0,1]
	v_fma_mix_f32 v154, v154, s42, -v157 op_sel_hi:[0,0,1]
	v_fma_mixlo_f16 v132, v130, s42, 0
	v_fma_mixlo_f16 v140, v138, s42, 0
	v_fma_mixlo_f16 v148, v146, s42, 0
	v_fma_mixlo_f16 v156, v154, s42, 0
	ds_write_b16 v204, v131
	ds_write_b16 v205, v139
	ds_write_b16 v206, v147
	ds_write_b16 v207, v155
	ds_write_b16 v204, v133 offset:544
	ds_write_b16 v205, v141 offset:544
	ds_write_b16 v206, v149 offset:544
	ds_write_b16 v207, v157 offset:544
	ds_write_b16 v204, v132 offset:1088
	ds_write_b16 v205, v140 offset:1088
	ds_write_b16 v206, v148 offset:1088
	ds_write_b16 v207, v156 offset:1088
	ds_read_b128 v[180:183], v199 offset:0
	s_waitcnt lgkmcnt(6)
	ds_read_b128 v[184:187], v199 offset:1024
	ds_read_b128 v[188:191], v199 offset:4096
	ds_read_b128 v[192:195], v199 offset:5120
	ds_read_b128 v[222:225], v199 offset:8192
	ds_read_b128 v[226:229], v199 offset:9216
	s_waitcnt lgkmcnt(0)
	s_barrier
	ds_read_b128 v[130:133], v208
	ds_read_b128 v[134:137], v209 offset:64
	ds_read_b128 v[138:141], v211
	ds_read_b128 v[142:145], v212
	ds_read_b128 v[146:149], v213
	ds_read_b128 v[150:153], v214
	ds_read_b128 v[154:157], v215
	ds_read_b128 v[158:161], v216
	s_waitcnt lgkmcnt(7)
	v_smfmac_f32_16x16x64_f16 v[230:233], v[130:133], a[16:23], v210
	v_smfmac_f32_16x16x64_f16 v[234:237], v[130:133], v[180:187], v210
	ds_read_b128 v[180:183], v199 offset:12288
	ds_read_b128 v[184:187], v199 offset:13312
	s_waitcnt lgkmcnt(8)
	v_smfmac_f32_16x16x64_f16 v[230:233], v[134:137], a[48:55], v210
	v_smfmac_f32_16x16x64_f16 v[234:237], v[134:137], v[188:195], v210
	ds_read_b128 v[188:191], v199 offset:16384
	ds_read_b128 v[192:195], v199 offset:17408
	s_waitcnt lgkmcnt(9)
	v_smfmac_f32_16x16x64_f16 v[230:233], v[138:141], a[80:87], v210
	v_smfmac_f32_16x16x64_f16 v[234:237], v[138:141], v[222:229], v210
	ds_read_b128 v[222:225], v199 offset:20480
	ds_read_b128 v[226:229], v199 offset:21504
	s_waitcnt lgkmcnt(10)
	v_smfmac_f32_16x16x64_f16 v[230:233], v[142:145], a[112:119], v210
	s_waitcnt lgkmcnt(4)
	v_smfmac_f32_16x16x64_f16 v[234:237], v[142:145], v[180:187], v210
	ds_read_b128 v[180:183], v199 offset:24576
	ds_read_b128 v[184:187], v199 offset:25600
	v_smfmac_f32_16x16x64_f16 v[230:233], v[146:149], a[144:151], v210
	s_waitcnt lgkmcnt(4)
	v_smfmac_f32_16x16x64_f16 v[234:237], v[146:149], v[188:195], v210
	ds_read_b128 v[188:191], v199 offset:28672
	ds_read_b128 v[192:195], v199 offset:29696
	v_smfmac_f32_16x16x64_f16 v[230:233], v[150:153], a[176:183], v210
	s_waitcnt lgkmcnt(4)
	v_smfmac_f32_16x16x64_f16 v[234:237], v[150:153], v[222:229], v210
	ds_read_b128 v[222:225], v199 offset:2048
	ds_read_b128 v[226:229], v199 offset:3072
	v_smfmac_f32_16x16x64_f16 v[230:233], v[154:157], a[208:215], v210
	s_waitcnt lgkmcnt(4)
	v_smfmac_f32_16x16x64_f16 v[234:237], v[154:157], v[180:187], v210
	ds_read_b128 v[180:183], v199 offset:6144
	ds_read_b128 v[184:187], v199 offset:7168
	s_waitcnt vmcnt(0)
	v_smfmac_f32_16x16x64_f16 v[230:233], v[158:161], a[240:247], v210
	s_waitcnt lgkmcnt(4)
	v_smfmac_f32_16x16x64_f16 v[234:237], v[158:161], v[188:195], v210
	ds_read_b128 v[188:191], v199 offset:10240
	ds_read_b128 v[192:195], v199 offset:11264
	v_smfmac_f32_16x16x64_f16 v[238:241], v[130:133], a[24:31], v210
	s_waitcnt lgkmcnt(4)
	v_smfmac_f32_16x16x64_f16 v[242:245], v[130:133], v[222:229], v210
	ds_read_b128 v[222:225], v199 offset:14336
	ds_read_b128 v[226:229], v199 offset:15360
	v_smfmac_f32_16x16x64_f16 v[238:241], v[134:137], a[56:63], v210
	v_fmac_f32_e32 v230, s40, v231
	s_waitcnt lgkmcnt(4)
	v_smfmac_f32_16x16x64_f16 v[242:245], v[134:137], v[180:187], v210
	ds_read_b128 v[180:183], v199 offset:18432
	ds_read_b128 v[184:187], v199 offset:19456
	v_fmac_f32_e32 v234, s40, v235
	v_smfmac_f32_16x16x64_f16 v[238:241], v[138:141], a[88:95], v210
	v_fmac_f32_e32 v230, s41, v232
	s_waitcnt lgkmcnt(4)
	v_smfmac_f32_16x16x64_f16 v[242:245], v[138:141], v[188:195], v210
	ds_read_b128 v[188:191], v199 offset:22528
	ds_read_b128 v[192:195], v199 offset:23552
	v_fmac_f32_e32 v234, s41, v236
	v_smfmac_f32_16x16x64_f16 v[238:241], v[142:145], a[120:127], v210
	s_nop 0
	v_permlane32_swap_b32_e32 v230, v234
	s_waitcnt lgkmcnt(4)
	v_smfmac_f32_16x16x64_f16 v[242:245], v[142:145], v[222:229], v210
	ds_read_b128 v[222:225], v199 offset:26624
	ds_read_b128 v[226:229], v199 offset:27648
	v_add_f32_e32 v175, v230, v234
	v_smfmac_f32_16x16x64_f16 v[238:241], v[146:149], a[152:159], v210
	ds_read_b128 v[230:233], v217
	s_waitcnt lgkmcnt(5)
	v_smfmac_f32_16x16x64_f16 v[242:245], v[146:149], v[180:187], v210
	ds_read_b128 v[180:183], v199 offset:30720
	ds_read_b128 v[184:187], v199 offset:31744
	ds_read_b128 v[234:237], v217
	v_smfmac_f32_16x16x64_f16 v[238:241], v[150:153], a[184:191], v210
	s_waitcnt lgkmcnt(6)
	v_smfmac_f32_16x16x64_f16 v[242:245], v[150:153], v[188:195], v210
	v_smfmac_f32_16x16x64_f16 v[238:241], v[154:157], a[216:223], v210
	s_waitcnt lgkmcnt(4)
	v_smfmac_f32_16x16x64_f16 v[242:245], v[154:157], v[222:229], v210
	v_smfmac_f32_16x16x64_f16 v[238:241], v[158:161], a[248:255], v210
	s_waitcnt lgkmcnt(1)
	v_smfmac_f32_16x16x64_f16 v[242:245], v[158:161], v[180:187], v210
	v_smfmac_f32_16x16x64_f16 v[230:233], v[130:133], a[0:7], v210
	s_waitcnt lgkmcnt(0)
	v_smfmac_f32_16x16x64_f16 v[234:237], v[130:133], v[18:25], v210
	v_smfmac_f32_16x16x64_f16 v[230:233], v[134:137], a[40:47], v210
	v_fmac_f32_e32 v238, s40, v239
	v_smfmac_f32_16x16x64_f16 v[234:237], v[134:137], v[34:41], v210
	v_fmac_f32_e32 v242, s40, v243
	v_smfmac_f32_16x16x64_f16 v[230:233], v[138:141], a[64:71], v210
	v_fmac_f32_e32 v238, s41, v240
	v_smfmac_f32_16x16x64_f16 v[234:237], v[138:141], v[42:49], v210
	v_fmac_f32_e32 v242, s41, v244
	v_smfmac_f32_16x16x64_f16 v[230:233], v[142:145], a[96:103], v210
	s_nop 0
	v_permlane32_swap_b32_e32 v238, v242
	v_smfmac_f32_16x16x64_f16 v[234:237], v[142:145], v[58:65], v210
	v_add_f32_e32 v174, v238, v242
	v_smfmac_f32_16x16x64_f16 v[230:233], v[146:149], a[128:135], v210
	ds_read_b128 v[238:241], v217
	v_smfmac_f32_16x16x64_f16 v[234:237], v[146:149], v[74:81], v210
	ds_read_b128 v[242:245], v217
	v_smfmac_f32_16x16x64_f16 v[230:233], v[150:153], a[160:167], v210
	v_smfmac_f32_16x16x64_f16 v[234:237], v[150:153], v[98:105], v210
	v_smfmac_f32_16x16x64_f16 v[230:233], v[154:157], a[192:199], v210
	v_smfmac_f32_16x16x64_f16 v[234:237], v[154:157], v[106:113], v210
	v_smfmac_f32_16x16x64_f16 v[230:233], v[158:161], a[224:231], v210
	v_smfmac_f32_16x16x64_f16 v[234:237], v[158:161], v[122:129], v210
	s_waitcnt lgkmcnt(1)
	v_smfmac_f32_16x16x64_f16 v[238:241], v[130:133], a[8:15], v210
	s_waitcnt lgkmcnt(0)
	v_smfmac_f32_16x16x64_f16 v[242:245], v[130:133], v[2:9], v210
	v_smfmac_f32_16x16x64_f16 v[238:241], v[134:137], a[32:39], v210
	v_fmac_f32_e32 v230, s40, v231
	v_smfmac_f32_16x16x64_f16 v[242:245], v[134:137], v[10:17], v210
	v_fmac_f32_e32 v234, s40, v235
	v_smfmac_f32_16x16x64_f16 v[238:241], v[138:141], a[72:79], v210
	v_fmac_f32_e32 v230, s41, v232
	v_smfmac_f32_16x16x64_f16 v[242:245], v[138:141], v[50:57], v210
	v_fmac_f32_e32 v234, s41, v236
	v_smfmac_f32_16x16x64_f16 v[238:241], v[142:145], a[104:111], v210
	s_nop 0
	v_permlane32_swap_b32_e32 v230, v234
	v_smfmac_f32_16x16x64_f16 v[242:245], v[142:145], v[26:33], v210
	v_add_f32_e32 v173, v230, v234
	v_smfmac_f32_16x16x64_f16 v[238:241], v[146:149], a[136:143], v210
	ds_read_b128 v[230:233], v217
	v_smfmac_f32_16x16x64_f16 v[242:245], v[146:149], v[82:89], v210
	ds_read_b128 v[234:237], v217
	v_smfmac_f32_16x16x64_f16 v[238:241], v[150:153], a[168:175], v210
	v_smfmac_f32_16x16x64_f16 v[242:245], v[150:153], v[66:73], v210
	v_smfmac_f32_16x16x64_f16 v[238:241], v[154:157], a[200:207], v210
	v_smfmac_f32_16x16x64_f16 v[242:245], v[154:157], v[114:121], v210
	v_smfmac_f32_16x16x64_f16 v[238:241], v[158:161], a[232:239], v210
	v_smfmac_f32_16x16x64_f16 v[242:245], v[158:161], v[90:97], v210
	s_nop 6
	v_fmac_f32_e32 v238, s40, v239
	v_fmac_f32_e32 v242, s40, v243
	v_fmac_f32_e32 v238, s41, v240
	v_fmac_f32_e32 v242, s41, v244
	s_nop 1
	v_permlane32_swap_b32_e32 v238, v242
	v_add_f32_e32 v172, v238, v242
	ds_read_b128 v[180:183], v199 offset:0
	ds_read_b128 v[184:187], v199 offset:1024
	ds_read_b128 v[188:191], v199 offset:4096
	ds_read_b128 v[192:195], v199 offset:5120
	ds_read_b128 v[222:225], v199 offset:8192
	ds_read_b128 v[226:229], v199 offset:9216
	s_mov_b32 s52, 0x3a83126f
	v_mov_b32_e32 v245, 0x358637bd
	v_fma_f32 v179, |v171|, s52, v245
	v_fma_f32 v196, |v170|, s52, v245
	v_fma_f32 v197, |v169|, s52, v245
	v_fma_f32 v198, |v168|, s52, v245
	v_rcp_f32_e32 v179, v179
	v_rcp_f32_e32 v196, v196
	v_rcp_f32_e32 v197, v197
	v_rcp_f32_e32 v198, v198
	v_mul_f32_e32 v238, v170, v196
	v_mul_f32_e32 v239, 0x3b000000, v172
	v_mul_f32_e32 v239, v239, v196
	v_mul_f32_e32 v130, v238, v238
	v_mul_f32_e32 v131, v239, v239
	v_mul_f32_e32 v238, v171, v179
	v_mul_f32_e32 v239, 0x3b000000, v173
	v_mul_f32_e32 v239, v239, v179
	v_fmac_f32_e32 v130, v238, v238
	v_fmac_f32_e32 v131, v239, v239
	v_mul_f32_e32 v238, v169, v197
	v_mul_f32_e32 v239, 0x3b000000, v175
	v_mul_f32_e32 v239, v239, v197
	v_fmac_f32_e32 v130, v238, v238
	v_fmac_f32_e32 v131, v239, v239
	v_mul_f32_e32 v238, v168, v198
	v_mul_f32_e32 v239, 0x3b000000, v174
	v_mul_f32_e32 v239, v239, v198
	v_fmac_f32_e32 v130, v238, v238
	v_fmac_f32_e32 v131, v239, v239
	s_nop 0
	v_add_f32_dpp v130, v130, v130 quad_perm:[1,0,3,2] row_mask:0xf bank_mask:0xf bound_ctrl:1
	v_add_f32_dpp v131, v131, v131 quad_perm:[1,0,3,2] row_mask:0xf bank_mask:0xf bound_ctrl:1
	s_nop 0
	v_add_f32_dpp v130, v130, v130 quad_perm:[2,3,0,1] row_mask:0xf bank_mask:0xf bound_ctrl:1
	v_add_f32_dpp v131, v131, v131 quad_perm:[2,3,0,1] row_mask:0xf bank_mask:0xf bound_ctrl:1
	s_nop 0
	v_add_f32_dpp v130, v130, v130 row_half_mirror row_mask:0xf bank_mask:0xf bound_ctrl:1
	v_add_f32_dpp v131, v131, v131 row_half_mirror row_mask:0xf bank_mask:0xf bound_ctrl:1
	s_nop 0
	v_add_f32_dpp v130, v130, v130 row_mirror row_mask:0xf bank_mask:0xf bound_ctrl:1
	v_add_f32_dpp v131, v131, v131 row_mirror row_mask:0xf bank_mask:0xf bound_ctrl:1
	v_mov_b32_e32 v240, v130
	v_mov_b32_e32 v241, v131
	s_nop 0
	v_permlane32_swap_b32_e32 v130, v240
	v_permlane32_swap_b32_e32 v131, v241
	v_add_f32_e32 v130, v130, v240
	v_add_f32_e32 v131, v131, v241
	v_add_u32_e32 v242, 0, v218
	v_lshlrev_b32_e32 v243, 3, v201
	v_or_b32_e32 v243, 0x24400, v243
	s_and_saveexec_b64 s[2:3], s[4:5]
	ds_write_b64 v242, v[130:131]
	s_or_b64 exec, exec, s[2:3]
	s_waitcnt lgkmcnt(0)
	s_barrier
	ds_read_b64 v[134:135], v243 offset:0
	ds_read_b64 v[138:139], v243 offset:16
	ds_read_b64 v[142:143], v243 offset:32
	ds_read_b64 v[146:147], v243 offset:48
	s_waitcnt lgkmcnt(2)
	v_add_f32_e32 v238, v134, v138
	s_waitcnt lgkmcnt(1)
	v_add_f32_e32 v238, v238, v142
	s_waitcnt lgkmcnt(0)
	v_add_f32_e32 v238, v238, v146
	v_add_f32_e32 v239, v135, v139
	v_add_f32_e32 v239, v239, v143
	v_add_f32_e32 v239, v239, v147
	v_mul_f32_e32 v238, 0x3b000000, v238
	v_max_f32_e32 v238, 0xda24260, v238
	v_sqrt_f32_e32 v238, v238
	v_mul_f32_e32 v239, 0x3b000000, v239
	v_max_f32_e32 v239, 0xda24260, v239
	v_sqrt_f32_e32 v239, v239
	s_nop 0
	v_mov_b32_e32 v220, v239
	v_rcp_f32_e32 v240, v239
	v_min_f32_e32 v241, v238, v239
	v_mul_f32_e32 v238, 0x3c23d70a, v238
	v_mul_f32_e32 v238, v238, v240
	s_mov_b32 s52, 0x3727c5ac
	v_cmp_ngt_f32_e32 vcc, s52, v241
	v_mov_b32_e32 v240, 0x358637bd
	s_nop 1
	v_cndmask_b32_e32 v219, v240, v238, vcc
	v_mul_f32_e32 v178, 0x3b000000, v219
	v_fma_mixlo_f16 v131, v178, v173, v171
	v_fma_mixlo_f16 v139, v178, v172, v170
	v_fma_mixlo_f16 v147, v178, v175, v169
	v_fma_mixlo_f16 v155, v178, v174, v168
	v_fma_f32 v130, v178, v173, v171
	v_fma_f32 v138, v178, v172, v170
	v_fma_f32 v146, v178, v175, v169
	v_fma_f32 v154, v178, v174, v168
	v_fma_mix_f32 v130, v130, 1.0, -v131 op_sel_hi:[0,0,1]
	v_fma_mix_f32 v138, v138, 1.0, -v139 op_sel_hi:[0,0,1]
	v_fma_mix_f32 v146, v146, 1.0, -v147 op_sel_hi:[0,0,1]
	v_fma_mix_f32 v154, v154, 1.0, -v155 op_sel_hi:[0,0,1]
	v_fma_mixlo_f16 v133, v130, s42, 0
	v_fma_mixlo_f16 v141, v138, s42, 0
	v_fma_mixlo_f16 v149, v146, s42, 0
	v_fma_mixlo_f16 v157, v154, s42, 0
	v_fma_mix_f32 v130, v130, s42, -v133 op_sel_hi:[0,0,1]
	v_fma_mix_f32 v138, v138, s42, -v141 op_sel_hi:[0,0,1]
	v_fma_mix_f32 v146, v146, s42, -v149 op_sel_hi:[0,0,1]
	v_fma_mix_f32 v154, v154, s42, -v157 op_sel_hi:[0,0,1]
	v_fma_mixlo_f16 v132, v130, s42, 0
	v_fma_mixlo_f16 v140, v138, s42, 0
	v_fma_mixlo_f16 v148, v146, s42, 0
	v_fma_mixlo_f16 v156, v154, s42, 0
	ds_write_b16 v204, v131 offset:8704
	ds_write_b16 v205, v139 offset:8704
	ds_write_b16 v206, v147 offset:8704
	ds_write_b16 v207, v155 offset:8704
	ds_write_b16 v204, v133 offset:9248
	ds_write_b16 v205, v141 offset:9248
	ds_write_b16 v206, v149 offset:9248
	ds_write_b16 v207, v157 offset:9248
	ds_write_b16 v204, v132 offset:9792
	ds_write_b16 v205, v140 offset:9792
	ds_write_b16 v206, v148 offset:9792
	ds_write_b16 v207, v156 offset:9792
	s_waitcnt lgkmcnt(0)
	s_barrier
	ds_read_b128 v[130:133], v208 offset:8704
	ds_read_b128 v[134:137], v209 offset:8768
	ds_read_b128 v[138:141], v211 offset:8704
	ds_read_b128 v[142:145], v212 offset:8704
	ds_read_b128 v[146:149], v213 offset:8704
	ds_read_b128 v[150:153], v214 offset:8704
	ds_read_b128 v[154:157], v215 offset:8704
	ds_read_b128 v[158:161], v216 offset:8704
	s_waitcnt lgkmcnt(7)
	v_smfmac_f32_16x16x64_f16 v[230:233], v[130:133], a[16:23], v210
	ds_read_b128 v[238:241], v217
	v_smfmac_f32_16x16x64_f16 v[234:237], v[130:133], v[180:187], v210
	ds_read_b128 v[180:183], v199 offset:12288
	ds_read_b128 v[184:187], v199 offset:13312
	ds_read_b128 v[242:245], v217
	s_waitcnt lgkmcnt(10)
	v_smfmac_f32_16x16x64_f16 v[230:233], v[134:137], a[48:55], v210
	v_smfmac_f32_16x16x64_f16 v[234:237], v[134:137], v[188:195], v210
	ds_read_b128 v[188:191], v199 offset:16384
	ds_read_b128 v[192:195], v199 offset:17408
	s_waitcnt lgkmcnt(11)
	v_smfmac_f32_16x16x64_f16 v[230:233], v[138:141], a[80:87], v210
	v_smfmac_f32_16x16x64_f16 v[234:237], v[138:141], v[222:229], v210
	ds_read_b128 v[222:225], v199 offset:20480
	ds_read_b128 v[226:229], v199 offset:21504
	s_waitcnt lgkmcnt(12)
	v_smfmac_f32_16x16x64_f16 v[230:233], v[142:145], a[112:119], v210
	s_waitcnt lgkmcnt(5)
	v_smfmac_f32_16x16x64_f16 v[234:237], v[142:145], v[180:187], v210
	ds_read_b128 v[180:183], v199 offset:24576
	ds_read_b128 v[184:187], v199 offset:25600
	v_smfmac_f32_16x16x64_f16 v[230:233], v[146:149], a[144:151], v210
	s_waitcnt lgkmcnt(4)
	v_smfmac_f32_16x16x64_f16 v[234:237], v[146:149], v[188:195], v210
	ds_read_b128 v[188:191], v199 offset:28672
	ds_read_b128 v[192:195], v199 offset:29696
	v_smfmac_f32_16x16x64_f16 v[230:233], v[150:153], a[176:183], v210
	s_waitcnt lgkmcnt(4)
	v_smfmac_f32_16x16x64_f16 v[234:237], v[150:153], v[222:229], v210
	ds_read_b128 v[222:225], v199 offset:2048
	ds_read_b128 v[226:229], v199 offset:3072
	v_smfmac_f32_16x16x64_f16 v[230:233], v[154:157], a[208:215], v210
	s_waitcnt lgkmcnt(4)
	v_smfmac_f32_16x16x64_f16 v[234:237], v[154:157], v[180:187], v210
	ds_read_b128 v[180:183], v199 offset:6144
	ds_read_b128 v[184:187], v199 offset:7168
	v_smfmac_f32_16x16x64_f16 v[230:233], v[158:161], a[240:247], v210
	s_waitcnt lgkmcnt(4)
	v_smfmac_f32_16x16x64_f16 v[234:237], v[158:161], v[188:195], v210
	ds_read_b128 v[188:191], v199 offset:10240
	ds_read_b128 v[192:195], v199 offset:11264
	v_smfmac_f32_16x16x64_f16 v[238:241], v[130:133], a[24:31], v210
	s_waitcnt lgkmcnt(4)
	v_smfmac_f32_16x16x64_f16 v[242:245], v[130:133], v[222:229], v210
	ds_read_b128 v[222:225], v199 offset:14336
	ds_read_b128 v[226:229], v199 offset:15360
	v_smfmac_f32_16x16x64_f16 v[238:241], v[134:137], a[56:63], v210
	v_fmac_f32_e32 v230, s40, v231
	s_waitcnt lgkmcnt(4)
	v_smfmac_f32_16x16x64_f16 v[242:245], v[134:137], v[180:187], v210
	ds_read_b128 v[180:183], v199 offset:18432
	ds_read_b128 v[184:187], v199 offset:19456
	v_fmac_f32_e32 v234, s40, v235
	v_smfmac_f32_16x16x64_f16 v[238:241], v[138:141], a[88:95], v210
	v_fmac_f32_e32 v230, s41, v232
	s_waitcnt lgkmcnt(4)
	v_smfmac_f32_16x16x64_f16 v[242:245], v[138:141], v[188:195], v210
	ds_read_b128 v[188:191], v199 offset:22528
	ds_read_b128 v[192:195], v199 offset:23552
	v_fmac_f32_e32 v234, s41, v236
	v_smfmac_f32_16x16x64_f16 v[238:241], v[142:145], a[120:127], v210
	s_nop 0
	v_permlane32_swap_b32_e32 v230, v234
	s_waitcnt lgkmcnt(4)
	v_smfmac_f32_16x16x64_f16 v[242:245], v[142:145], v[222:229], v210
	ds_read_b128 v[222:225], v199 offset:26624
	ds_read_b128 v[226:229], v199 offset:27648
	v_add_f32_e32 v164, v230, v234
	v_smfmac_f32_16x16x64_f16 v[238:241], v[146:149], a[152:159], v210
	ds_read_b128 v[230:233], v217
	s_waitcnt lgkmcnt(5)
	v_smfmac_f32_16x16x64_f16 v[242:245], v[146:149], v[180:187], v210
	ds_read_b128 v[180:183], v199 offset:30720
	ds_read_b128 v[184:187], v199 offset:31744
	ds_read_b128 v[234:237], v217
	v_smfmac_f32_16x16x64_f16 v[238:241], v[150:153], a[184:191], v210
	s_waitcnt lgkmcnt(6)
	v_smfmac_f32_16x16x64_f16 v[242:245], v[150:153], v[188:195], v210
	v_smfmac_f32_16x16x64_f16 v[238:241], v[154:157], a[216:223], v210
	s_waitcnt lgkmcnt(4)
	v_smfmac_f32_16x16x64_f16 v[242:245], v[154:157], v[222:229], v210
	v_smfmac_f32_16x16x64_f16 v[238:241], v[158:161], a[248:255], v210
	s_waitcnt lgkmcnt(1)
	v_smfmac_f32_16x16x64_f16 v[242:245], v[158:161], v[180:187], v210
	v_smfmac_f32_16x16x64_f16 v[230:233], v[130:133], a[0:7], v210
	s_waitcnt lgkmcnt(0)
	v_smfmac_f32_16x16x64_f16 v[234:237], v[130:133], v[18:25], v210
	v_smfmac_f32_16x16x64_f16 v[230:233], v[134:137], a[40:47], v210
	v_fmac_f32_e32 v238, s40, v239
	v_smfmac_f32_16x16x64_f16 v[234:237], v[134:137], v[34:41], v210
	v_fmac_f32_e32 v242, s40, v243
	v_smfmac_f32_16x16x64_f16 v[230:233], v[138:141], a[64:71], v210
	v_fmac_f32_e32 v238, s41, v240
	v_smfmac_f32_16x16x64_f16 v[234:237], v[138:141], v[42:49], v210
	v_fmac_f32_e32 v242, s41, v244
	v_smfmac_f32_16x16x64_f16 v[230:233], v[142:145], a[96:103], v210
	s_nop 0
	v_permlane32_swap_b32_e32 v238, v242
	v_smfmac_f32_16x16x64_f16 v[234:237], v[142:145], v[58:65], v210
	v_add_f32_e32 v165, v238, v242
	v_smfmac_f32_16x16x64_f16 v[230:233], v[146:149], a[128:135], v210
	ds_read_b128 v[238:241], v217
	v_smfmac_f32_16x16x64_f16 v[234:237], v[146:149], v[74:81], v210
	ds_read_b128 v[242:245], v217
	v_smfmac_f32_16x16x64_f16 v[230:233], v[150:153], a[160:167], v210
	v_smfmac_f32_16x16x64_f16 v[234:237], v[150:153], v[98:105], v210
	v_smfmac_f32_16x16x64_f16 v[230:233], v[154:157], a[192:199], v210
	v_smfmac_f32_16x16x64_f16 v[234:237], v[154:157], v[106:113], v210
	v_smfmac_f32_16x16x64_f16 v[230:233], v[158:161], a[224:231], v210
	v_smfmac_f32_16x16x64_f16 v[234:237], v[158:161], v[122:129], v210
	s_waitcnt lgkmcnt(1)
	v_smfmac_f32_16x16x64_f16 v[238:241], v[130:133], a[8:15], v210
	s_waitcnt lgkmcnt(0)
	v_smfmac_f32_16x16x64_f16 v[242:245], v[130:133], v[2:9], v210
	v_smfmac_f32_16x16x64_f16 v[238:241], v[134:137], a[32:39], v210
	v_fmac_f32_e32 v230, s40, v231
	v_smfmac_f32_16x16x64_f16 v[242:245], v[134:137], v[10:17], v210
	v_fmac_f32_e32 v234, s40, v235
	v_smfmac_f32_16x16x64_f16 v[238:241], v[138:141], a[72:79], v210
	v_fmac_f32_e32 v230, s41, v232
	v_smfmac_f32_16x16x64_f16 v[242:245], v[138:141], v[50:57], v210
	v_fmac_f32_e32 v234, s41, v236
	v_smfmac_f32_16x16x64_f16 v[238:241], v[142:145], a[104:111], v210
	s_nop 0
	v_permlane32_swap_b32_e32 v230, v234
	v_smfmac_f32_16x16x64_f16 v[242:245], v[142:145], v[26:33], v210
	v_add_f32_e32 v162, v230, v234
	v_smfmac_f32_16x16x64_f16 v[238:241], v[146:149], a[136:143], v210
	ds_read_b128 v[230:233], v217
	v_smfmac_f32_16x16x64_f16 v[242:245], v[146:149], v[82:89], v210
	ds_read_b128 v[234:237], v217
	v_smfmac_f32_16x16x64_f16 v[238:241], v[150:153], a[168:175], v210
	v_smfmac_f32_16x16x64_f16 v[242:245], v[150:153], v[66:73], v210
	v_smfmac_f32_16x16x64_f16 v[238:241], v[154:157], a[200:207], v210
	v_smfmac_f32_16x16x64_f16 v[242:245], v[154:157], v[114:121], v210
	v_smfmac_f32_16x16x64_f16 v[238:241], v[158:161], a[232:239], v210
	v_smfmac_f32_16x16x64_f16 v[242:245], v[158:161], v[90:97], v210
	s_nop 6
	v_fmac_f32_e32 v238, s40, v239
	v_fmac_f32_e32 v242, s40, v243
	v_fmac_f32_e32 v238, s41, v240
	v_fmac_f32_e32 v242, s41, v244
	s_nop 1
	v_permlane32_swap_b32_e32 v238, v242
	v_add_f32_e32 v163, v238, v242
	ds_read_b128 v[180:183], v199 offset:0
	ds_read_b128 v[184:187], v199 offset:1024
	ds_read_b128 v[188:191], v199 offset:4096
	ds_read_b128 v[192:195], v199 offset:5120
	ds_read_b128 v[222:225], v199 offset:8192
	ds_read_b128 v[226:229], v199 offset:9216
	v_sub_f32_e32 v238, v163, v172
	v_mul_f32_e32 v238, 0x3b000000, v238
	v_mul_f32_e32 v238, v238, v196
	v_mul_f32_e32 v130, v238, v238
	v_sub_f32_e32 v238, v162, v173
	v_mul_f32_e32 v238, 0x3b000000, v238
	v_mul_f32_e32 v238, v238, v179
	v_fmac_f32_e32 v130, v238, v238
	v_sub_f32_e32 v238, v164, v175
	v_mul_f32_e32 v238, 0x3b000000, v238
	v_mul_f32_e32 v238, v238, v197
	v_fmac_f32_e32 v130, v238, v238
	v_sub_f32_e32 v238, v165, v174
	v_mul_f32_e32 v238, 0x3b000000, v238
	v_mul_f32_e32 v238, v238, v198
	v_fmac_f32_e32 v130, v238, v238
	s_nop 1
	v_add_f32_dpp v130, v130, v130 quad_perm:[1,0,3,2] row_mask:0xf bank_mask:0xf bound_ctrl:1
	s_nop 1
	v_add_f32_dpp v130, v130, v130 quad_perm:[2,3,0,1] row_mask:0xf bank_mask:0xf bound_ctrl:1
	s_nop 1
	v_add_f32_dpp v130, v130, v130 row_half_mirror row_mask:0xf bank_mask:0xf bound_ctrl:1
	s_nop 1
	v_add_f32_dpp v130, v130, v130 row_mirror row_mask:0xf bank_mask:0xf bound_ctrl:1
	v_mov_b32_e32 v240, v130
	s_nop 1
	v_permlane32_swap_b32_e32 v130, v240
	v_add_f32_e32 v130, v130, v240
	v_add_u32_e32 v242, 64, v218
	v_lshlrev_b32_e32 v243, 3, v201
	v_or_b32_e32 v243, 0x24440, v243
	s_and_saveexec_b64 s[2:3], s[4:5]
	ds_write_b32 v242, v130
	s_or_b64 exec, exec, s[2:3]
	s_waitcnt lgkmcnt(0)
	s_barrier
	ds_read2_b32 v[134:135], v243 offset1:4
	ds_read2_b32 v[136:137], v243 offset0:8 offset1:12
	s_waitcnt lgkmcnt(1)
	v_add_f32_e32 v238, v134, v135
	s_waitcnt lgkmcnt(0)
	v_add_f32_e32 v238, v238, v136
	v_add_f32_e32 v238, v238, v137
	v_mul_f32_e32 v238, 0x3b000000, v238
	v_max_f32_e32 v238, 0xda24260, v238
	v_rcp_f32_e32 v240, v219
	v_sqrt_f32_e32 v238, v238
	s_nop 0
	v_mul_f32_e32 v238, v240, v238
	v_max_f32_e32 v241, v220, v238
	v_mul_f32_e32 v242, 0x3a83126f, v219
	v_max_f32_e32 v242, 0x358637bd, v242
	v_max_f32_e32 v243, 0x26901d7d, v241
	v_rcp_f32_e32 v243, v243
	s_nop 0
	v_mul_f32_e32 v243, 0x3c23d70a, v243
	v_log_f32_e32 v243, v243
	s_nop 0
	v_mul_f32_e32 v243, 0x3e4ccccd, v243
	v_exp_f32_e32 v243, v243
	s_mov_b32 s52, 0x26901d7d
	v_cmp_ge_f32_e32 vcc, s52, v241
	s_nop 1
	v_cndmask_b32_e32 v243, v243, v242, vcc
	v_mul_f32_e32 v242, 0x42c80000, v219
	v_min3_f32 v1, v242, v243, 1.0
.Lrk_top:
	v_sub_f32_e32 v238, 1.0, v221
	v_min_f32_e32 v178, v1, v238
	v_cmp_eq_f32_e32 vcc, 0, v178
	v_mul_f32_e32 v178, 0x3b000000, v178
	s_cmp_eq_u64 vcc, exec
	s_cbranch_scc1 .Lrk_exit
	s_cmp_gt_i32 s30, 63
	s_cbranch_scc1 .Lrk_exit
	v_mul_f32_e32 v134, 0x3e4ccccd, v173
	v_mul_f32_e32 v142, 0x3e4ccccd, v172
	v_mul_f32_e32 v150, 0x3e4ccccd, v175
	v_mul_f32_e32 v158, 0x3e4ccccd, v174
	v_fma_mixlo_f16 v131, v178, v134, v171
	v_fma_mixlo_f16 v139, v178, v142, v170
	v_fma_mixlo_f16 v147, v178, v150, v169
	v_fma_mixlo_f16 v155, v178, v158, v168
	v_fma_f32 v130, v178, v134, v171
	v_fma_f32 v138, v178, v142, v170
	v_fma_f32 v146, v178, v150, v169
	v_fma_f32 v154, v178, v158, v168
	v_fma_mix_f32 v130, v130, 1.0, -v131 op_sel_hi:[0,0,1]
	v_fma_mix_f32 v138, v138, 1.0, -v139 op_sel_hi:[0,0,1]
	v_fma_mix_f32 v146, v146, 1.0, -v147 op_sel_hi:[0,0,1]
	v_fma_mix_f32 v154, v154, 1.0, -v155 op_sel_hi:[0,0,1]
	v_fma_mixlo_f16 v133, v130, s42, 0
	v_fma_mixlo_f16 v141, v138, s42, 0
	v_fma_mixlo_f16 v149, v146, s42, 0
	v_fma_mixlo_f16 v157, v154, s42, 0
	v_fma_mix_f32 v130, v130, s42, -v133 op_sel_hi:[0,0,1]
	v_fma_mix_f32 v138, v138, s42, -v141 op_sel_hi:[0,0,1]
	v_fma_mix_f32 v146, v146, s42, -v149 op_sel_hi:[0,0,1]
	v_fma_mix_f32 v154, v154, s42, -v157 op_sel_hi:[0,0,1]
	v_fma_mixlo_f16 v132, v130, s42, 0
	v_fma_mixlo_f16 v140, v138, s42, 0
	v_fma_mixlo_f16 v148, v146, s42, 0
	v_fma_mixlo_f16 v156, v154, s42, 0
	ds_write_b16 v204, v131
	ds_write_b16 v205, v139
	ds_write_b16 v206, v147
	ds_write_b16 v207, v155
	ds_write_b16 v204, v133 offset:544
	ds_write_b16 v205, v141 offset:544
	ds_write_b16 v206, v149 offset:544
	ds_write_b16 v207, v157 offset:544
	ds_write_b16 v204, v132 offset:1088
	ds_write_b16 v205, v140 offset:1088
	ds_write_b16 v206, v148 offset:1088
	ds_write_b16 v207, v156 offset:1088
	s_waitcnt lgkmcnt(0)
	s_barrier
	ds_read_b128 v[130:133], v208
	ds_read_b128 v[134:137], v209 offset:64
	ds_read_b128 v[138:141], v211
	ds_read_b128 v[142:145], v212
	ds_read_b128 v[146:149], v213
	ds_read_b128 v[150:153], v214
	ds_read_b128 v[154:157], v215
	ds_read_b128 v[158:161], v216
	s_waitcnt lgkmcnt(7)
	v_smfmac_f32_16x16x64_f16 v[230:233], v[130:133], a[16:23], v210
	ds_read_b128 v[238:241], v217
	v_smfmac_f32_16x16x64_f16 v[234:237], v[130:133], v[180:187], v210
	ds_read_b128 v[180:183], v199 offset:12288
	ds_read_b128 v[184:187], v199 offset:13312
	ds_read_b128 v[242:245], v217
	s_waitcnt lgkmcnt(10)
	v_smfmac_f32_16x16x64_f16 v[230:233], v[134:137], a[48:55], v210
	v_mul_f32_e32 v166, 0x3d99999a, v173
	v_smfmac_f32_16x16x64_f16 v[234:237], v[134:137], v[188:195], v210
	ds_read_b128 v[188:191], v199 offset:16384
	ds_read_b128 v[192:195], v199 offset:17408
	v_mul_f32_e32 v167, 0x3d99999a, v172
	s_waitcnt lgkmcnt(11)
	v_smfmac_f32_16x16x64_f16 v[230:233], v[138:141], a[80:87], v210
	v_mul_f32_e32 v176, 0x3d99999a, v175
	v_smfmac_f32_16x16x64_f16 v[234:237], v[138:141], v[222:229], v210
	ds_read_b128 v[222:225], v199 offset:20480
	ds_read_b128 v[226:229], v199 offset:21504
	v_mul_f32_e32 v177, 0x3d99999a, v174
	s_waitcnt lgkmcnt(12)
	v_smfmac_f32_16x16x64_f16 v[230:233], v[142:145], a[112:119], v210
	s_waitcnt lgkmcnt(5)
	v_smfmac_f32_16x16x64_f16 v[234:237], v[142:145], v[180:187], v210
	ds_read_b128 v[180:183], v199 offset:24576
	ds_read_b128 v[184:187], v199 offset:25600
	v_smfmac_f32_16x16x64_f16 v[230:233], v[146:149], a[144:151], v210
	s_waitcnt lgkmcnt(4)
	v_smfmac_f32_16x16x64_f16 v[234:237], v[146:149], v[188:195], v210
	ds_read_b128 v[188:191], v199 offset:28672
	ds_read_b128 v[192:195], v199 offset:29696
	v_smfmac_f32_16x16x64_f16 v[230:233], v[150:153], a[176:183], v210
	s_waitcnt lgkmcnt(4)
	v_smfmac_f32_16x16x64_f16 v[234:237], v[150:153], v[222:229], v210
	ds_read_b128 v[222:225], v199 offset:2048
	ds_read_b128 v[226:229], v199 offset:3072
	v_smfmac_f32_16x16x64_f16 v[230:233], v[154:157], a[208:215], v210
	s_waitcnt lgkmcnt(4)
	v_smfmac_f32_16x16x64_f16 v[234:237], v[154:157], v[180:187], v210
	ds_read_b128 v[180:183], v199 offset:6144
	ds_read_b128 v[184:187], v199 offset:7168
	v_smfmac_f32_16x16x64_f16 v[230:233], v[158:161], a[240:247], v210
	s_waitcnt lgkmcnt(4)
	v_smfmac_f32_16x16x64_f16 v[234:237], v[158:161], v[188:195], v210
	ds_read_b128 v[188:191], v199 offset:10240
	ds_read_b128 v[192:195], v199 offset:11264
	v_smfmac_f32_16x16x64_f16 v[238:241], v[130:133], a[24:31], v210
	s_waitcnt lgkmcnt(4)
	v_smfmac_f32_16x16x64_f16 v[242:245], v[130:133], v[222:229], v210
	ds_read_b128 v[222:225], v199 offset:14336
	ds_read_b128 v[226:229], v199 offset:15360
	v_smfmac_f32_16x16x64_f16 v[238:241], v[134:137], a[56:63], v210
	v_fmac_f32_e32 v230, s40, v231
	v_fmac_f32_e32 v234, s40, v235
	s_waitcnt lgkmcnt(4)
	v_smfmac_f32_16x16x64_f16 v[242:245], v[134:137], v[180:187], v210
	ds_read_b128 v[180:183], v199 offset:18432
	ds_read_b128 v[184:187], v199 offset:19456
	v_fmac_f32_e32 v230, s41, v232
	v_fmac_f32_e32 v234, s41, v236
	v_smfmac_f32_16x16x64_f16 v[238:241], v[138:141], a[88:95], v210
	s_nop 0
	v_permlane32_swap_b32_e32 v230, v234
	v_add_f32_e32 v164, v230, v234
	s_waitcnt lgkmcnt(4)
	v_smfmac_f32_16x16x64_f16 v[242:245], v[138:141], v[188:195], v210
	ds_read_b128 v[188:191], v199 offset:22528
	ds_read_b128 v[192:195], v199 offset:23552
	v_fmac_f32_e32 v176, 0x3e666666, v164
	v_fma_mixlo_f16 v232, v178, v176, v169
	v_smfmac_f32_16x16x64_f16 v[238:241], v[142:145], a[120:127], v210
	v_fma_f32 v231, v178, v176, v169
	v_fma_mix_f32 v231, v231, 1.0, -v232 op_sel_hi:[0,0,1]
	s_waitcnt lgkmcnt(4)
	v_smfmac_f32_16x16x64_f16 v[242:245], v[142:145], v[222:229], v210
	ds_read_b128 v[222:225], v199 offset:26624
	ds_read_b128 v[226:229], v199 offset:27648
	v_fma_mixlo_f16 v235, v231, s42, 0
	v_smfmac_f32_16x16x64_f16 v[238:241], v[146:149], a[152:159], v210
	v_fma_mix_f32 v231, v231, s42, -v235 op_sel_hi:[0,0,1]
	s_waitcnt lgkmcnt(4)
	v_smfmac_f32_16x16x64_f16 v[242:245], v[146:149], v[180:187], v210
	ds_read_b128 v[180:183], v199 offset:30720
	ds_read_b128 v[184:187], v199 offset:31744
	v_fma_mixlo_f16 v233, v231, s42, 0
	v_smfmac_f32_16x16x64_f16 v[238:241], v[150:153], a[184:191], v210
	ds_write_b16 v206, v232 offset:8704
	s_waitcnt lgkmcnt(5)
	v_smfmac_f32_16x16x64_f16 v[242:245], v[150:153], v[188:195], v210
	ds_write_b16 v206, v235 offset:9248
	v_smfmac_f32_16x16x64_f16 v[238:241], v[154:157], a[216:223], v210
	ds_write_b16 v206, v233 offset:9792
	s_waitcnt lgkmcnt(5)
	v_smfmac_f32_16x16x64_f16 v[242:245], v[154:157], v[222:229], v210
	ds_read_b128 v[230:233], v217
	v_smfmac_f32_16x16x64_f16 v[238:241], v[158:161], a[248:255], v210
	ds_read_b128 v[234:237], v217
	s_waitcnt lgkmcnt(5)
	v_smfmac_f32_16x16x64_f16 v[242:245], v[158:161], v[180:187], v210
	s_waitcnt lgkmcnt(1)
	v_smfmac_f32_16x16x64_f16 v[230:233], v[130:133], a[0:7], v210
	s_waitcnt lgkmcnt(0)
	v_smfmac_f32_16x16x64_f16 v[234:237], v[130:133], v[18:25], v210
	v_smfmac_f32_16x16x64_f16 v[230:233], v[134:137], a[40:47], v210
	v_fmac_f32_e32 v238, s40, v239
	v_fmac_f32_e32 v242, s40, v243
	v_smfmac_f32_16x16x64_f16 v[234:237], v[134:137], v[34:41], v210
	v_fmac_f32_e32 v238, s41, v240
	v_fmac_f32_e32 v242, s41, v244
	v_smfmac_f32_16x16x64_f16 v[230:233], v[138:141], a[64:71], v210
	s_nop 0
	v_permlane32_swap_b32_e32 v238, v242
	v_add_f32_e32 v165, v238, v242
	v_smfmac_f32_16x16x64_f16 v[234:237], v[138:141], v[42:49], v210
	v_fmac_f32_e32 v177, 0x3e666666, v165
	v_fma_mixlo_f16 v240, v178, v177, v168
	v_smfmac_f32_16x16x64_f16 v[230:233], v[142:145], a[96:103], v210
	v_fma_f32 v239, v178, v177, v168
	v_fma_mix_f32 v239, v239, 1.0, -v240 op_sel_hi:[0,0,1]
	v_smfmac_f32_16x16x64_f16 v[234:237], v[142:145], v[58:65], v210
	v_fma_mixlo_f16 v243, v239, s42, 0
	v_smfmac_f32_16x16x64_f16 v[230:233], v[146:149], a[128:135], v210
	v_fma_mix_f32 v239, v239, s42, -v243 op_sel_hi:[0,0,1]
	v_smfmac_f32_16x16x64_f16 v[234:237], v[146:149], v[74:81], v210
	v_fma_mixlo_f16 v241, v239, s42, 0
	v_smfmac_f32_16x16x64_f16 v[230:233], v[150:153], a[160:167], v210
	ds_write_b16 v207, v240 offset:8704
	v_smfmac_f32_16x16x64_f16 v[234:237], v[150:153], v[98:105], v210
	ds_write_b16 v207, v243 offset:9248
	v_smfmac_f32_16x16x64_f16 v[230:233], v[154:157], a[192:199], v210
	ds_write_b16 v207, v241 offset:9792
	v_smfmac_f32_16x16x64_f16 v[234:237], v[154:157], v[106:113], v210
	ds_read_b128 v[238:241], v217
	v_smfmac_f32_16x16x64_f16 v[230:233], v[158:161], a[224:231], v210
	ds_read_b128 v[242:245], v217
	v_smfmac_f32_16x16x64_f16 v[234:237], v[158:161], v[122:129], v210
	s_waitcnt lgkmcnt(1)
	v_smfmac_f32_16x16x64_f16 v[238:241], v[130:133], a[8:15], v210
	s_waitcnt lgkmcnt(0)
	v_smfmac_f32_16x16x64_f16 v[242:245], v[130:133], v[2:9], v210
	v_smfmac_f32_16x16x64_f16 v[238:241], v[134:137], a[32:39], v210
	v_fmac_f32_e32 v230, s40, v231
	v_fmac_f32_e32 v234, s40, v235
	v_smfmac_f32_16x16x64_f16 v[242:245], v[134:137], v[10:17], v210
	v_fmac_f32_e32 v230, s41, v232
	v_fmac_f32_e32 v234, s41, v236
	v_smfmac_f32_16x16x64_f16 v[238:241], v[138:141], a[72:79], v210
	s_nop 0
	v_permlane32_swap_b32_e32 v230, v234
	v_add_f32_e32 v162, v230, v234
	v_smfmac_f32_16x16x64_f16 v[242:245], v[138:141], v[50:57], v210
	v_fmac_f32_e32 v166, 0x3e666666, v162
	v_fma_mixlo_f16 v232, v178, v166, v171
	v_smfmac_f32_16x16x64_f16 v[238:241], v[142:145], a[104:111], v210
	v_fma_f32 v231, v178, v166, v171
	v_fma_mix_f32 v231, v231, 1.0, -v232 op_sel_hi:[0,0,1]
	v_smfmac_f32_16x16x64_f16 v[242:245], v[142:145], v[26:33], v210
	v_fma_mixlo_f16 v235, v231, s42, 0
	v_smfmac_f32_16x16x64_f16 v[238:241], v[146:149], a[136:143], v210
	v_fma_mix_f32 v231, v231, s42, -v235 op_sel_hi:[0,0,1]
	v_smfmac_f32_16x16x64_f16 v[242:245], v[146:149], v[82:89], v210
	v_fma_mixlo_f16 v233, v231, s42, 0
	v_smfmac_f32_16x16x64_f16 v[238:241], v[150:153], a[168:175], v210
	ds_write_b16 v204, v232 offset:8704
	v_smfmac_f32_16x16x64_f16 v[242:245], v[150:153], v[66:73], v210
	ds_write_b16 v204, v235 offset:9248
	v_smfmac_f32_16x16x64_f16 v[238:241], v[154:157], a[200:207], v210
	ds_write_b16 v204, v233 offset:9792
	v_smfmac_f32_16x16x64_f16 v[242:245], v[154:157], v[114:121], v210
	ds_read_b128 v[230:233], v217
	v_smfmac_f32_16x16x64_f16 v[238:241], v[158:161], a[232:239], v210
	ds_read_b128 v[234:237], v217
	v_smfmac_f32_16x16x64_f16 v[242:245], v[158:161], v[90:97], v210
	s_nop 5
	v_fmac_f32_e32 v238, s40, v239
	s_nop 0
	v_fmac_f32_e32 v242, s40, v243
	v_fmac_f32_e32 v238, s41, v240
	v_fmac_f32_e32 v242, s41, v244
	s_nop 1
	v_permlane32_swap_b32_e32 v238, v242
	v_add_f32_e32 v163, v238, v242
	v_fmac_f32_e32 v167, 0x3e666666, v163
	v_fma_mixlo_f16 v240, v178, v167, v170
	v_fma_f32 v239, v178, v167, v170
	v_fma_mix_f32 v239, v239, 1.0, -v240 op_sel_hi:[0,0,1]
	v_fma_mixlo_f16 v243, v239, s42, 0
	v_fma_mix_f32 v239, v239, s42, -v243 op_sel_hi:[0,0,1]
	v_fma_mixlo_f16 v241, v239, s42, 0
	ds_write_b16 v205, v240 offset:8704
	ds_write_b16 v205, v243 offset:9248
	ds_write_b16 v205, v241 offset:9792
	ds_read_b128 v[180:183], v199 offset:0
	ds_read_b128 v[184:187], v199 offset:1024
	ds_read_b128 v[188:191], v199 offset:4096
	ds_read_b128 v[192:195], v199 offset:5120
	ds_read_b128 v[222:225], v199 offset:8192
	s_waitcnt lgkmcnt(6)
	ds_read_b128 v[226:229], v199 offset:9216
	s_waitcnt lgkmcnt(0)
	s_barrier
	ds_read_b128 v[130:133], v208 offset:8704
	ds_read_b128 v[134:137], v209 offset:8768
	ds_read_b128 v[138:141], v211 offset:8704
	ds_read_b128 v[142:145], v212 offset:8704
	ds_read_b128 v[146:149], v213 offset:8704
	ds_read_b128 v[150:153], v214 offset:8704
	ds_read_b128 v[154:157], v215 offset:8704
	ds_read_b128 v[158:161], v216 offset:8704
	s_waitcnt lgkmcnt(7)
	v_smfmac_f32_16x16x64_f16 v[230:233], v[130:133], a[16:23], v210
	ds_read_b128 v[238:241], v217
	v_smfmac_f32_16x16x64_f16 v[234:237], v[130:133], v[180:187], v210
	ds_read_b128 v[180:183], v199 offset:12288
	ds_read_b128 v[184:187], v199 offset:13312
	ds_read_b128 v[242:245], v217
	s_waitcnt lgkmcnt(10)
	v_smfmac_f32_16x16x64_f16 v[230:233], v[134:137], a[48:55], v210
	v_mul_f32_e32 v179, 0x3f7a4fa5, v173
	v_smfmac_f32_16x16x64_f16 v[234:237], v[134:137], v[188:195], v210
	ds_read_b128 v[188:191], v199 offset:16384
	ds_read_b128 v[192:195], v199 offset:17408
	v_fmac_f32_e32 v179, 0xc06eeeef, v162
	s_waitcnt lgkmcnt(11)
	v_smfmac_f32_16x16x64_f16 v[230:233], v[138:141], a[80:87], v210
	v_mul_f32_e32 v196, 0x3f7a4fa5, v172
	v_smfmac_f32_16x16x64_f16 v[234:237], v[138:141], v[222:229], v210
	ds_read_b128 v[222:225], v199 offset:20480
	ds_read_b128 v[226:229], v199 offset:21504
	v_fmac_f32_e32 v196, 0xc06eeeef, v163
	s_waitcnt lgkmcnt(12)
	v_smfmac_f32_16x16x64_f16 v[230:233], v[142:145], a[112:119], v210
	v_mul_f32_e32 v197, 0x3f7a4fa5, v175
	s_waitcnt lgkmcnt(5)
	v_smfmac_f32_16x16x64_f16 v[234:237], v[142:145], v[180:187], v210
	ds_read_b128 v[180:183], v199 offset:24576
	ds_read_b128 v[184:187], v199 offset:25600
	v_fmac_f32_e32 v197, 0xc06eeeef, v164
	v_smfmac_f32_16x16x64_f16 v[230:233], v[146:149], a[144:151], v210
	v_mul_f32_e32 v198, 0x3f7a4fa5, v174
	s_waitcnt lgkmcnt(4)
	v_smfmac_f32_16x16x64_f16 v[234:237], v[146:149], v[188:195], v210
	ds_read_b128 v[188:191], v199 offset:28672
	ds_read_b128 v[192:195], v199 offset:29696
	v_fmac_f32_e32 v198, 0xc06eeeef, v165
	v_smfmac_f32_16x16x64_f16 v[230:233], v[150:153], a[176:183], v210
	s_waitcnt lgkmcnt(4)
	v_smfmac_f32_16x16x64_f16 v[234:237], v[150:153], v[222:229], v210
	ds_read_b128 v[222:225], v199 offset:2048
	ds_read_b128 v[226:229], v199 offset:3072
	v_smfmac_f32_16x16x64_f16 v[230:233], v[154:157], a[208:215], v210
	s_waitcnt lgkmcnt(4)
	v_smfmac_f32_16x16x64_f16 v[234:237], v[154:157], v[180:187], v210
	ds_read_b128 v[180:183], v199 offset:6144
	ds_read_b128 v[184:187], v199 offset:7168
	v_smfmac_f32_16x16x64_f16 v[230:233], v[158:161], a[240:247], v210
	s_waitcnt lgkmcnt(4)
	v_smfmac_f32_16x16x64_f16 v[234:237], v[158:161], v[188:195], v210
	ds_read_b128 v[188:191], v199 offset:10240
	ds_read_b128 v[192:195], v199 offset:11264
	v_smfmac_f32_16x16x64_f16 v[238:241], v[130:133], a[24:31], v210
	s_waitcnt lgkmcnt(4)
	v_smfmac_f32_16x16x64_f16 v[242:245], v[130:133], v[222:229], v210
	ds_read_b128 v[222:225], v199 offset:14336
	ds_read_b128 v[226:229], v199 offset:15360
	v_smfmac_f32_16x16x64_f16 v[238:241], v[134:137], a[56:63], v210
	v_fmac_f32_e32 v230, s40, v231
	v_fmac_f32_e32 v234, s40, v235
	s_waitcnt lgkmcnt(4)
	v_smfmac_f32_16x16x64_f16 v[242:245], v[134:137], v[180:187], v210
	ds_read_b128 v[180:183], v199 offset:18432
	ds_read_b128 v[184:187], v199 offset:19456
	v_fmac_f32_e32 v230, s41, v232
	v_fmac_f32_e32 v234, s41, v236
	v_smfmac_f32_16x16x64_f16 v[238:241], v[138:141], a[88:95], v210
	s_nop 0
	v_permlane32_swap_b32_e32 v230, v234
	v_add_f32_e32 v176, v230, v234
	s_waitcnt lgkmcnt(4)
	v_smfmac_f32_16x16x64_f16 v[242:245], v[138:141], v[188:195], v210
	ds_read_b128 v[188:191], v199 offset:22528
	ds_read_b128 v[192:195], v199 offset:23552
	v_fmac_f32_e32 v197, 0x40638e39, v176
	v_fma_mixlo_f16 v232, v178, v197, v169
	v_smfmac_f32_16x16x64_f16 v[238:241], v[142:145], a[120:127], v210
	v_fma_f32 v231, v178, v197, v169
	v_fma_mix_f32 v231, v231, 1.0, -v232 op_sel_hi:[0,0,1]
	s_waitcnt lgkmcnt(4)
	v_smfmac_f32_16x16x64_f16 v[242:245], v[142:145], v[222:229], v210
	ds_read_b128 v[222:225], v199 offset:26624
	ds_read_b128 v[226:229], v199 offset:27648
	v_fma_mixlo_f16 v235, v231, s42, 0
	v_smfmac_f32_16x16x64_f16 v[238:241], v[146:149], a[152:159], v210
	v_fma_mix_f32 v231, v231, s42, -v235 op_sel_hi:[0,0,1]
	s_waitcnt lgkmcnt(4)
	v_smfmac_f32_16x16x64_f16 v[242:245], v[146:149], v[180:187], v210
	ds_read_b128 v[180:183], v199 offset:30720
	ds_read_b128 v[184:187], v199 offset:31744
	v_fma_mixlo_f16 v233, v231, s42, 0
	v_smfmac_f32_16x16x64_f16 v[238:241], v[150:153], a[184:191], v210
	ds_write_b16 v206, v232
	s_waitcnt lgkmcnt(5)
	v_smfmac_f32_16x16x64_f16 v[242:245], v[150:153], v[188:195], v210
	ds_write_b16 v206, v235 offset:544
	v_smfmac_f32_16x16x64_f16 v[238:241], v[154:157], a[216:223], v210
	ds_write_b16 v206, v233 offset:1088
	s_waitcnt lgkmcnt(5)
	v_smfmac_f32_16x16x64_f16 v[242:245], v[154:157], v[222:229], v210
	ds_read_b128 v[230:233], v217
	v_smfmac_f32_16x16x64_f16 v[238:241], v[158:161], a[248:255], v210
	ds_read_b128 v[234:237], v217
	s_waitcnt lgkmcnt(5)
	v_smfmac_f32_16x16x64_f16 v[242:245], v[158:161], v[180:187], v210
	s_waitcnt lgkmcnt(1)
	v_smfmac_f32_16x16x64_f16 v[230:233], v[130:133], a[0:7], v210
	s_waitcnt lgkmcnt(0)
	v_smfmac_f32_16x16x64_f16 v[234:237], v[130:133], v[18:25], v210
	v_smfmac_f32_16x16x64_f16 v[230:233], v[134:137], a[40:47], v210
	v_fmac_f32_e32 v238, s40, v239
	v_fmac_f32_e32 v242, s40, v243
	v_smfmac_f32_16x16x64_f16 v[234:237], v[134:137], v[34:41], v210
	v_fmac_f32_e32 v238, s41, v240
	v_fmac_f32_e32 v242, s41, v244
	v_smfmac_f32_16x16x64_f16 v[230:233], v[138:141], a[64:71], v210
	s_nop 0
	v_permlane32_swap_b32_e32 v238, v242
	v_add_f32_e32 v177, v238, v242
	v_smfmac_f32_16x16x64_f16 v[234:237], v[138:141], v[42:49], v210
	v_fmac_f32_e32 v198, 0x40638e39, v177
	v_fma_mixlo_f16 v240, v178, v198, v168
	v_smfmac_f32_16x16x64_f16 v[230:233], v[142:145], a[96:103], v210
	v_fma_f32 v239, v178, v198, v168
	v_fma_mix_f32 v239, v239, 1.0, -v240 op_sel_hi:[0,0,1]
	v_smfmac_f32_16x16x64_f16 v[234:237], v[142:145], v[58:65], v210
	v_fma_mixlo_f16 v243, v239, s42, 0
	v_smfmac_f32_16x16x64_f16 v[230:233], v[146:149], a[128:135], v210
	v_fma_mix_f32 v239, v239, s42, -v243 op_sel_hi:[0,0,1]
	v_smfmac_f32_16x16x64_f16 v[234:237], v[146:149], v[74:81], v210
	v_fma_mixlo_f16 v241, v239, s42, 0
	v_smfmac_f32_16x16x64_f16 v[230:233], v[150:153], a[160:167], v210
	ds_write_b16 v207, v240
	v_smfmac_f32_16x16x64_f16 v[234:237], v[150:153], v[98:105], v210
	ds_write_b16 v207, v243 offset:544
	v_smfmac_f32_16x16x64_f16 v[230:233], v[154:157], a[192:199], v210
	ds_write_b16 v207, v241 offset:1088
	v_smfmac_f32_16x16x64_f16 v[234:237], v[154:157], v[106:113], v210
	ds_read_b128 v[238:241], v217
	v_smfmac_f32_16x16x64_f16 v[230:233], v[158:161], a[224:231], v210
	ds_read_b128 v[242:245], v217
	v_smfmac_f32_16x16x64_f16 v[234:237], v[158:161], v[122:129], v210
	s_waitcnt lgkmcnt(1)
	v_smfmac_f32_16x16x64_f16 v[238:241], v[130:133], a[8:15], v210
	s_waitcnt lgkmcnt(0)
	v_smfmac_f32_16x16x64_f16 v[242:245], v[130:133], v[2:9], v210
	v_smfmac_f32_16x16x64_f16 v[238:241], v[134:137], a[32:39], v210
	v_fmac_f32_e32 v230, s40, v231
	v_fmac_f32_e32 v234, s40, v235
	v_smfmac_f32_16x16x64_f16 v[242:245], v[134:137], v[10:17], v210
	v_fmac_f32_e32 v230, s41, v232
	v_fmac_f32_e32 v234, s41, v236
	v_smfmac_f32_16x16x64_f16 v[238:241], v[138:141], a[72:79], v210
	s_nop 0
	v_permlane32_swap_b32_e32 v230, v234
	v_add_f32_e32 v166, v230, v234
	v_smfmac_f32_16x16x64_f16 v[242:245], v[138:141], v[50:57], v210
	v_fmac_f32_e32 v179, 0x40638e39, v166
	v_fma_mixlo_f16 v232, v178, v179, v171
	v_smfmac_f32_16x16x64_f16 v[238:241], v[142:145], a[104:111], v210
	v_fma_f32 v231, v178, v179, v171
	v_fma_mix_f32 v231, v231, 1.0, -v232 op_sel_hi:[0,0,1]
	v_smfmac_f32_16x16x64_f16 v[242:245], v[142:145], v[26:33], v210
	v_fma_mixlo_f16 v235, v231, s42, 0
	v_smfmac_f32_16x16x64_f16 v[238:241], v[146:149], a[136:143], v210
	v_fma_mix_f32 v231, v231, s42, -v235 op_sel_hi:[0,0,1]
	v_smfmac_f32_16x16x64_f16 v[242:245], v[146:149], v[82:89], v210
	v_fma_mixlo_f16 v233, v231, s42, 0
	v_smfmac_f32_16x16x64_f16 v[238:241], v[150:153], a[168:175], v210
	ds_write_b16 v204, v232
	v_smfmac_f32_16x16x64_f16 v[242:245], v[150:153], v[66:73], v210
	ds_write_b16 v204, v235 offset:544
	v_smfmac_f32_16x16x64_f16 v[238:241], v[154:157], a[200:207], v210
	ds_write_b16 v204, v233 offset:1088
	v_smfmac_f32_16x16x64_f16 v[242:245], v[154:157], v[114:121], v210
	ds_read_b128 v[230:233], v217
	v_smfmac_f32_16x16x64_f16 v[238:241], v[158:161], a[232:239], v210
	ds_read_b128 v[234:237], v217
	v_smfmac_f32_16x16x64_f16 v[242:245], v[158:161], v[90:97], v210
	s_nop 5
	v_fmac_f32_e32 v238, s40, v239
	s_nop 0
	v_fmac_f32_e32 v242, s40, v243
	v_fmac_f32_e32 v238, s41, v240
	v_fmac_f32_e32 v242, s41, v244
	s_nop 1
	v_permlane32_swap_b32_e32 v238, v242
	v_add_f32_e32 v167, v238, v242
	v_fmac_f32_e32 v196, 0x40638e39, v167
	v_fma_mixlo_f16 v240, v178, v196, v170
	v_fma_f32 v239, v178, v196, v170
	v_fma_mix_f32 v239, v239, 1.0, -v240 op_sel_hi:[0,0,1]
	v_fma_mixlo_f16 v243, v239, s42, 0
	v_fma_mix_f32 v239, v239, s42, -v243 op_sel_hi:[0,0,1]
	v_fma_mixlo_f16 v241, v239, s42, 0
	ds_write_b16 v205, v240
	ds_write_b16 v205, v243 offset:544
	ds_write_b16 v205, v241 offset:1088
	ds_read_b128 v[180:183], v199 offset:0
	ds_read_b128 v[184:187], v199 offset:1024
	ds_read_b128 v[188:191], v199 offset:4096
	ds_read_b128 v[192:195], v199 offset:5120
	ds_read_b128 v[222:225], v199 offset:8192
	s_waitcnt lgkmcnt(6)
	ds_read_b128 v[226:229], v199 offset:9216
	s_waitcnt lgkmcnt(0)
	s_barrier
	ds_read_b128 v[130:133], v208
	ds_read_b128 v[134:137], v209 offset:64
	ds_read_b128 v[138:141], v211
	ds_read_b128 v[142:145], v212
	ds_read_b128 v[146:149], v213
	ds_read_b128 v[150:153], v214
	ds_read_b128 v[154:157], v215
	ds_read_b128 v[158:161], v216
	s_waitcnt lgkmcnt(7)
	v_smfmac_f32_16x16x64_f16 v[230:233], v[130:133], a[16:23], v210
	ds_read_b128 v[238:241], v217
	v_smfmac_f32_16x16x64_f16 v[234:237], v[130:133], v[180:187], v210
	ds_read_b128 v[180:183], v199 offset:12288
	ds_read_b128 v[184:187], v199 offset:13312
	ds_read_b128 v[242:245], v217
	s_waitcnt lgkmcnt(10)
	v_smfmac_f32_16x16x64_f16 v[230:233], v[134:137], a[48:55], v210
	v_mul_f32_e32 v219, 0x403cf760, v173
	v_smfmac_f32_16x16x64_f16 v[234:237], v[134:137], v[188:195], v210
	ds_read_b128 v[188:191], v199 offset:16384
	ds_read_b128 v[192:195], v199 offset:17408
	v_fmac_f32_e32 v219, 0xc139885f, v162
	s_waitcnt lgkmcnt(11)
	v_smfmac_f32_16x16x64_f16 v[230:233], v[138:141], a[80:87], v210
	v_fmac_f32_e32 v219, 0x411d2a92, v166
	v_smfmac_f32_16x16x64_f16 v[234:237], v[138:141], v[222:229], v210
	ds_read_b128 v[222:225], v199 offset:20480
	ds_read_b128 v[226:229], v199 offset:21504
	v_mul_f32_e32 v220, 0x403cf760, v172
	s_waitcnt lgkmcnt(12)
	v_smfmac_f32_16x16x64_f16 v[230:233], v[142:145], a[112:119], v210
	v_fmac_f32_e32 v220, 0xc139885f, v163
	s_waitcnt lgkmcnt(5)
	v_smfmac_f32_16x16x64_f16 v[234:237], v[142:145], v[180:187], v210
	ds_read_b128 v[180:183], v199 offset:24576
	ds_read_b128 v[184:187], v199 offset:25600
	v_fmac_f32_e32 v220, 0x411d2a92, v167
	v_smfmac_f32_16x16x64_f16 v[230:233], v[146:149], a[144:151], v210
	v_mul_f32_e32 v246, 0x403cf760, v175
	s_waitcnt lgkmcnt(4)
	v_smfmac_f32_16x16x64_f16 v[234:237], v[146:149], v[188:195], v210
	ds_read_b128 v[188:191], v199 offset:28672
	ds_read_b128 v[192:195], v199 offset:29696
	v_fmac_f32_e32 v246, 0xc139885f, v164
	v_smfmac_f32_16x16x64_f16 v[230:233], v[150:153], a[176:183], v210
	v_fmac_f32_e32 v246, 0x411d2a92, v176
	s_waitcnt lgkmcnt(4)
	v_smfmac_f32_16x16x64_f16 v[234:237], v[150:153], v[222:229], v210
	ds_read_b128 v[222:225], v199 offset:2048
	ds_read_b128 v[226:229], v199 offset:3072
	v_mul_f32_e32 v247, 0x403cf760, v174
	v_smfmac_f32_16x16x64_f16 v[230:233], v[154:157], a[208:215], v210
	v_fmac_f32_e32 v247, 0xc139885f, v165
	s_waitcnt lgkmcnt(4)
	v_smfmac_f32_16x16x64_f16 v[234:237], v[154:157], v[180:187], v210
	ds_read_b128 v[180:183], v199 offset:6144
	ds_read_b128 v[184:187], v199 offset:7168
	v_fmac_f32_e32 v247, 0x411d2a92, v177
	v_smfmac_f32_16x16x64_f16 v[230:233], v[158:161], a[240:247], v210
	s_waitcnt lgkmcnt(4)
	v_smfmac_f32_16x16x64_f16 v[234:237], v[158:161], v[188:195], v210
	ds_read_b128 v[188:191], v199 offset:10240
	ds_read_b128 v[192:195], v199 offset:11264
	v_smfmac_f32_16x16x64_f16 v[238:241], v[130:133], a[24:31], v210
	s_waitcnt lgkmcnt(4)
	v_smfmac_f32_16x16x64_f16 v[242:245], v[130:133], v[222:229], v210
	ds_read_b128 v[222:225], v199 offset:14336
	ds_read_b128 v[226:229], v199 offset:15360
	v_smfmac_f32_16x16x64_f16 v[238:241], v[134:137], a[56:63], v210
	v_fmac_f32_e32 v230, s40, v231
	v_fmac_f32_e32 v234, s40, v235
	s_waitcnt lgkmcnt(4)
	v_smfmac_f32_16x16x64_f16 v[242:245], v[134:137], v[180:187], v210
	ds_read_b128 v[180:183], v199 offset:18432
	ds_read_b128 v[184:187], v199 offset:19456
	v_fmac_f32_e32 v230, s41, v232
	v_fmac_f32_e32 v234, s41, v236
	v_smfmac_f32_16x16x64_f16 v[238:241], v[138:141], a[88:95], v210
	s_nop 0
	v_permlane32_swap_b32_e32 v230, v234
	v_add_f32_e32 v197, v230, v234
	s_waitcnt lgkmcnt(4)
	v_smfmac_f32_16x16x64_f16 v[242:245], v[138:141], v[188:195], v210
	ds_read_b128 v[188:191], v199 offset:22528
	ds_read_b128 v[192:195], v199 offset:23552
	v_fmac_f32_e32 v246, 0xbe94e4f6, v197
	v_fma_mixlo_f16 v232, v178, v246, v169
	v_smfmac_f32_16x16x64_f16 v[238:241], v[142:145], a[120:127], v210
	v_fma_f32 v231, v178, v246, v169
	v_fma_mix_f32 v231, v231, 1.0, -v232 op_sel_hi:[0,0,1]
	s_waitcnt lgkmcnt(4)
	v_smfmac_f32_16x16x64_f16 v[242:245], v[142:145], v[222:229], v210
	ds_read_b128 v[222:225], v199 offset:26624
	ds_read_b128 v[226:229], v199 offset:27648
	v_fma_mixlo_f16 v235, v231, s42, 0
	v_smfmac_f32_16x16x64_f16 v[238:241], v[146:149], a[152:159], v210
	v_fma_mix_f32 v231, v231, s42, -v235 op_sel_hi:[0,0,1]
	s_waitcnt lgkmcnt(4)
	v_smfmac_f32_16x16x64_f16 v[242:245], v[146:149], v[180:187], v210
	ds_read_b128 v[180:183], v199 offset:30720
	ds_read_b128 v[184:187], v199 offset:31744
	v_fma_mixlo_f16 v233, v231, s42, 0
	v_smfmac_f32_16x16x64_f16 v[238:241], v[150:153], a[184:191], v210
	ds_write_b16 v206, v232 offset:8704
	s_waitcnt lgkmcnt(5)
	v_smfmac_f32_16x16x64_f16 v[242:245], v[150:153], v[188:195], v210
	ds_write_b16 v206, v235 offset:9248
	v_smfmac_f32_16x16x64_f16 v[238:241], v[154:157], a[216:223], v210
	ds_write_b16 v206, v233 offset:9792
	s_waitcnt lgkmcnt(5)
	v_smfmac_f32_16x16x64_f16 v[242:245], v[154:157], v[222:229], v210
	ds_read_b128 v[230:233], v217
	v_smfmac_f32_16x16x64_f16 v[238:241], v[158:161], a[248:255], v210
	ds_read_b128 v[234:237], v217
	s_waitcnt lgkmcnt(5)
	v_smfmac_f32_16x16x64_f16 v[242:245], v[158:161], v[180:187], v210
	s_waitcnt lgkmcnt(1)
	v_smfmac_f32_16x16x64_f16 v[230:233], v[130:133], a[0:7], v210
	s_waitcnt lgkmcnt(0)
	v_smfmac_f32_16x16x64_f16 v[234:237], v[130:133], v[18:25], v210
	v_smfmac_f32_16x16x64_f16 v[230:233], v[134:137], a[40:47], v210
	v_fmac_f32_e32 v238, s40, v239
	v_fmac_f32_e32 v242, s40, v243
	v_smfmac_f32_16x16x64_f16 v[234:237], v[134:137], v[34:41], v210
	v_fmac_f32_e32 v238, s41, v240
	v_fmac_f32_e32 v242, s41, v244
	v_smfmac_f32_16x16x64_f16 v[230:233], v[138:141], a[64:71], v210
	s_nop 0
	v_permlane32_swap_b32_e32 v238, v242
	v_add_f32_e32 v198, v238, v242
	v_smfmac_f32_16x16x64_f16 v[234:237], v[138:141], v[42:49], v210
	v_fmac_f32_e32 v247, 0xbe94e4f6, v198
	v_fma_mixlo_f16 v240, v178, v247, v168
	v_smfmac_f32_16x16x64_f16 v[230:233], v[142:145], a[96:103], v210
	v_fma_f32 v239, v178, v247, v168
	v_fma_mix_f32 v239, v239, 1.0, -v240 op_sel_hi:[0,0,1]
	v_smfmac_f32_16x16x64_f16 v[234:237], v[142:145], v[58:65], v210
	v_fma_mixlo_f16 v243, v239, s42, 0
	v_smfmac_f32_16x16x64_f16 v[230:233], v[146:149], a[128:135], v210
	v_fma_mix_f32 v239, v239, s42, -v243 op_sel_hi:[0,0,1]
	v_smfmac_f32_16x16x64_f16 v[234:237], v[146:149], v[74:81], v210
	v_fma_mixlo_f16 v241, v239, s42, 0
	v_smfmac_f32_16x16x64_f16 v[230:233], v[150:153], a[160:167], v210
	ds_write_b16 v207, v240 offset:8704
	v_smfmac_f32_16x16x64_f16 v[234:237], v[150:153], v[98:105], v210
	ds_write_b16 v207, v243 offset:9248
	v_smfmac_f32_16x16x64_f16 v[230:233], v[154:157], a[192:199], v210
	ds_write_b16 v207, v241 offset:9792
	v_smfmac_f32_16x16x64_f16 v[234:237], v[154:157], v[106:113], v210
	ds_read_b128 v[238:241], v217
	v_smfmac_f32_16x16x64_f16 v[230:233], v[158:161], a[224:231], v210
	ds_read_b128 v[242:245], v217
	v_smfmac_f32_16x16x64_f16 v[234:237], v[158:161], v[122:129], v210
	s_waitcnt lgkmcnt(1)
	v_smfmac_f32_16x16x64_f16 v[238:241], v[130:133], a[8:15], v210
	s_waitcnt lgkmcnt(0)
	v_smfmac_f32_16x16x64_f16 v[242:245], v[130:133], v[2:9], v210
	v_smfmac_f32_16x16x64_f16 v[238:241], v[134:137], a[32:39], v210
	v_fmac_f32_e32 v230, s40, v231
	v_fmac_f32_e32 v234, s40, v235
	v_smfmac_f32_16x16x64_f16 v[242:245], v[134:137], v[10:17], v210
	v_fmac_f32_e32 v230, s41, v232
	v_fmac_f32_e32 v234, s41, v236
	v_smfmac_f32_16x16x64_f16 v[238:241], v[138:141], a[72:79], v210
	s_nop 0
	v_permlane32_swap_b32_e32 v230, v234
	v_add_f32_e32 v179, v230, v234
	v_smfmac_f32_16x16x64_f16 v[242:245], v[138:141], v[50:57], v210
	v_fmac_f32_e32 v219, 0xbe94e4f6, v179
	v_fma_mixlo_f16 v232, v178, v219, v171
	v_smfmac_f32_16x16x64_f16 v[238:241], v[142:145], a[104:111], v210
	v_fma_f32 v231, v178, v219, v171
	v_fma_mix_f32 v231, v231, 1.0, -v232 op_sel_hi:[0,0,1]
	v_smfmac_f32_16x16x64_f16 v[242:245], v[142:145], v[26:33], v210
	v_fma_mixlo_f16 v235, v231, s42, 0
	v_smfmac_f32_16x16x64_f16 v[238:241], v[146:149], a[136:143], v210
	v_fma_mix_f32 v231, v231, s42, -v235 op_sel_hi:[0,0,1]
	v_smfmac_f32_16x16x64_f16 v[242:245], v[146:149], v[82:89], v210
	v_fma_mixlo_f16 v233, v231, s42, 0
	v_smfmac_f32_16x16x64_f16 v[238:241], v[150:153], a[168:175], v210
	ds_write_b16 v204, v232 offset:8704
	v_smfmac_f32_16x16x64_f16 v[242:245], v[150:153], v[66:73], v210
	ds_write_b16 v204, v235 offset:9248
	v_smfmac_f32_16x16x64_f16 v[238:241], v[154:157], a[200:207], v210
	ds_write_b16 v204, v233 offset:9792
	v_smfmac_f32_16x16x64_f16 v[242:245], v[154:157], v[114:121], v210
	ds_read_b128 v[230:233], v217
	v_smfmac_f32_16x16x64_f16 v[238:241], v[158:161], a[232:239], v210
	ds_read_b128 v[234:237], v217
	v_smfmac_f32_16x16x64_f16 v[242:245], v[158:161], v[90:97], v210
	s_nop 5
	v_fmac_f32_e32 v238, s40, v239
	s_nop 0
	v_fmac_f32_e32 v242, s40, v243
	v_fmac_f32_e32 v238, s41, v240
	v_fmac_f32_e32 v242, s41, v244
	s_nop 1
	v_permlane32_swap_b32_e32 v238, v242
	v_add_f32_e32 v196, v238, v242
	v_fmac_f32_e32 v220, 0xbe94e4f6, v196
	v_fma_mixlo_f16 v240, v178, v220, v170
	v_fma_f32 v239, v178, v220, v170
	v_fma_mix_f32 v239, v239, 1.0, -v240 op_sel_hi:[0,0,1]
	v_fma_mixlo_f16 v243, v239, s42, 0
	v_fma_mix_f32 v239, v239, s42, -v243 op_sel_hi:[0,0,1]
	v_fma_mixlo_f16 v241, v239, s42, 0
	ds_write_b16 v205, v240 offset:8704
	ds_write_b16 v205, v243 offset:9248
	ds_write_b16 v205, v241 offset:9792
	ds_read_b128 v[180:183], v199 offset:0
	ds_read_b128 v[184:187], v199 offset:1024
	ds_read_b128 v[188:191], v199 offset:4096
	ds_read_b128 v[192:195], v199 offset:5120
	ds_read_b128 v[222:225], v199 offset:8192
	s_waitcnt lgkmcnt(6)
	ds_read_b128 v[226:229], v199 offset:9216
	s_waitcnt lgkmcnt(0)
	s_barrier
	ds_read_b128 v[130:133], v208 offset:8704
	ds_read_b128 v[134:137], v209 offset:8768
	ds_read_b128 v[138:141], v211 offset:8704
	ds_read_b128 v[142:145], v212 offset:8704
	ds_read_b128 v[146:149], v213 offset:8704
	ds_read_b128 v[150:153], v214 offset:8704
	ds_read_b128 v[154:157], v215 offset:8704
	ds_read_b128 v[158:161], v216 offset:8704
	s_waitcnt lgkmcnt(7)
	v_smfmac_f32_16x16x64_f16 v[230:233], v[130:133], a[16:23], v210
	ds_read_b128 v[238:241], v217
	ds_read_b128 v[242:245], v217
	v_smfmac_f32_16x16x64_f16 v[234:237], v[130:133], v[180:187], v210
	ds_read_b128 v[180:183], v199 offset:12288
	ds_read_b128 v[184:187], v199 offset:13312
	v_mul_f32_e32 v248, 0x40362960, v173
	v_fmac_f32_e32 v248, 0xc12c1f08, v162
	s_waitcnt lgkmcnt(10)
	v_smfmac_f32_16x16x64_f16 v[230:233], v[134:137], a[48:55], v210
	v_fmac_f32_e32 v248, 0x410e80b5, v166
	v_fmac_f32_e32 v248, 0x3e8e8ba3, v179
	v_smfmac_f32_16x16x64_f16 v[234:237], v[134:137], v[188:195], v210
	ds_read_b128 v[188:191], v199 offset:16384
	ds_read_b128 v[192:195], v199 offset:17408
	v_mul_f32_e32 v249, 0x40362960, v172
	s_waitcnt lgkmcnt(11)
	v_smfmac_f32_16x16x64_f16 v[230:233], v[138:141], a[80:87], v210
	v_fmac_f32_e32 v249, 0xc12c1f08, v163
	v_smfmac_f32_16x16x64_f16 v[234:237], v[138:141], v[222:229], v210
	ds_read_b128 v[222:225], v199 offset:20480
	ds_read_b128 v[226:229], v199 offset:21504
	v_fmac_f32_e32 v249, 0x410e80b5, v167
	s_waitcnt lgkmcnt(12)
	v_smfmac_f32_16x16x64_f16 v[230:233], v[142:145], a[112:119], v210
	v_fmac_f32_e32 v249, 0x3e8e8ba3, v196
	s_waitcnt lgkmcnt(4)
	v_smfmac_f32_16x16x64_f16 v[234:237], v[142:145], v[180:187], v210
	ds_read_b128 v[180:183], v199 offset:24576
	ds_read_b128 v[184:187], v199 offset:25600
	v_mul_f32_e32 v250, 0x40362960, v175
	v_smfmac_f32_16x16x64_f16 v[230:233], v[146:149], a[144:151], v210
	v_fmac_f32_e32 v250, 0xc12c1f08, v164
	s_waitcnt lgkmcnt(4)
	v_smfmac_f32_16x16x64_f16 v[234:237], v[146:149], v[188:195], v210
	ds_read_b128 v[188:191], v199 offset:28672
	ds_read_b128 v[192:195], v199 offset:29696
	v_fmac_f32_e32 v250, 0x410e80b5, v176
	v_smfmac_f32_16x16x64_f16 v[230:233], v[150:153], a[176:183], v210
	v_fmac_f32_e32 v250, 0x3e8e8ba3, v197
	s_waitcnt lgkmcnt(4)
	v_smfmac_f32_16x16x64_f16 v[234:237], v[150:153], v[222:229], v210
	ds_read_b128 v[222:225], v199 offset:2048
	ds_read_b128 v[226:229], v199 offset:3072
	v_mul_f32_e32 v251, 0x40362960, v174
	v_smfmac_f32_16x16x64_f16 v[230:233], v[154:157], a[208:215], v210
	v_fmac_f32_e32 v251, 0xc12c1f08, v165
	s_waitcnt lgkmcnt(4)
	v_smfmac_f32_16x16x64_f16 v[234:237], v[154:157], v[180:187], v210
	ds_read_b128 v[180:183], v199 offset:6144
	ds_read_b128 v[184:187], v199 offset:7168
	v_fmac_f32_e32 v251, 0x410e80b5, v177
	v_smfmac_f32_16x16x64_f16 v[230:233], v[158:161], a[240:247], v210
	v_fmac_f32_e32 v251, 0x3e8e8ba3, v198
	s_waitcnt lgkmcnt(4)
	v_smfmac_f32_16x16x64_f16 v[234:237], v[158:161], v[188:195], v210
	ds_read_b128 v[188:191], v199 offset:10240
	ds_read_b128 v[192:195], v199 offset:11264
	v_smfmac_f32_16x16x64_f16 v[238:241], v[130:133], a[24:31], v210
	s_waitcnt lgkmcnt(4)
	v_smfmac_f32_16x16x64_f16 v[242:245], v[130:133], v[222:229], v210
	ds_read_b128 v[222:225], v199 offset:14336
	ds_read_b128 v[226:229], v199 offset:15360
	v_smfmac_f32_16x16x64_f16 v[238:241], v[134:137], a[56:63], v210
	v_fmac_f32_e32 v230, s40, v231
	v_fmac_f32_e32 v234, s40, v235
	s_waitcnt lgkmcnt(4)
	v_smfmac_f32_16x16x64_f16 v[242:245], v[134:137], v[180:187], v210
	ds_read_b128 v[180:183], v199 offset:18432
	ds_read_b128 v[184:187], v199 offset:19456
	v_fmac_f32_e32 v230, s41, v232
	v_fmac_f32_e32 v234, s41, v236
	v_smfmac_f32_16x16x64_f16 v[238:241], v[138:141], a[88:95], v210
	s_nop 0
	v_permlane32_swap_b32_e32 v230, v234
	v_add_f32_e32 v246, v230, v234
	s_waitcnt lgkmcnt(4)
	v_smfmac_f32_16x16x64_f16 v[242:245], v[138:141], v[188:195], v210
	ds_read_b128 v[188:191], v199 offset:22528
	ds_read_b128 v[192:195], v199 offset:23552
	v_fmac_f32_e32 v250, 0xbe8c0c4c, v246
	v_fma_mixlo_f16 v232, v178, v250, v169
	v_smfmac_f32_16x16x64_f16 v[238:241], v[142:145], a[120:127], v210
	v_fma_f32 v231, v178, v250, v169
	v_fma_mix_f32 v231, v231, 1.0, -v232 op_sel_hi:[0,0,1]
	s_waitcnt lgkmcnt(4)
	v_smfmac_f32_16x16x64_f16 v[242:245], v[142:145], v[222:229], v210
	ds_read_b128 v[222:225], v199 offset:26624
	ds_read_b128 v[226:229], v199 offset:27648
	v_fma_mixlo_f16 v235, v231, s42, 0
	v_smfmac_f32_16x16x64_f16 v[238:241], v[146:149], a[152:159], v210
	v_fma_mix_f32 v231, v231, s42, -v235 op_sel_hi:[0,0,1]
	s_waitcnt lgkmcnt(4)
	v_smfmac_f32_16x16x64_f16 v[242:245], v[146:149], v[180:187], v210
	ds_read_b128 v[180:183], v199 offset:30720
	ds_read_b128 v[184:187], v199 offset:31744
	v_fma_mixlo_f16 v233, v231, s42, 0
	v_smfmac_f32_16x16x64_f16 v[238:241], v[150:153], a[184:191], v210
	ds_write_b16 v206, v232
	s_waitcnt lgkmcnt(5)
	v_smfmac_f32_16x16x64_f16 v[242:245], v[150:153], v[188:195], v210
	ds_write_b16 v206, v235 offset:544
	v_smfmac_f32_16x16x64_f16 v[238:241], v[154:157], a[216:223], v210
	ds_write_b16 v206, v233 offset:1088
	s_waitcnt lgkmcnt(5)
	v_smfmac_f32_16x16x64_f16 v[242:245], v[154:157], v[222:229], v210
	ds_read_b128 v[230:233], v217
	v_smfmac_f32_16x16x64_f16 v[238:241], v[158:161], a[248:255], v210
	ds_read_b128 v[234:237], v217
	s_waitcnt lgkmcnt(5)
	v_smfmac_f32_16x16x64_f16 v[242:245], v[158:161], v[180:187], v210
	s_waitcnt lgkmcnt(1)
	v_smfmac_f32_16x16x64_f16 v[230:233], v[130:133], a[0:7], v210
	s_waitcnt lgkmcnt(0)
	v_smfmac_f32_16x16x64_f16 v[234:237], v[130:133], v[18:25], v210
	v_smfmac_f32_16x16x64_f16 v[230:233], v[134:137], a[40:47], v210
	v_fmac_f32_e32 v238, s40, v239
	v_fmac_f32_e32 v242, s40, v243
	v_smfmac_f32_16x16x64_f16 v[234:237], v[134:137], v[34:41], v210
	v_fmac_f32_e32 v238, s41, v240
	v_fmac_f32_e32 v242, s41, v244
	v_smfmac_f32_16x16x64_f16 v[230:233], v[138:141], a[64:71], v210
	s_nop 0
	v_permlane32_swap_b32_e32 v238, v242
	v_add_f32_e32 v247, v238, v242
	v_smfmac_f32_16x16x64_f16 v[234:237], v[138:141], v[42:49], v210
	v_fmac_f32_e32 v251, 0xbe8c0c4c, v247
	v_fma_mixlo_f16 v240, v178, v251, v168
	v_smfmac_f32_16x16x64_f16 v[230:233], v[142:145], a[96:103], v210
	v_fma_f32 v239, v178, v251, v168
	v_fma_mix_f32 v239, v239, 1.0, -v240 op_sel_hi:[0,0,1]
	v_smfmac_f32_16x16x64_f16 v[234:237], v[142:145], v[58:65], v210
	v_fma_mixlo_f16 v243, v239, s42, 0
	v_smfmac_f32_16x16x64_f16 v[230:233], v[146:149], a[128:135], v210
	v_fma_mix_f32 v239, v239, s42, -v243 op_sel_hi:[0,0,1]
	v_smfmac_f32_16x16x64_f16 v[234:237], v[146:149], v[74:81], v210
	v_fma_mixlo_f16 v241, v239, s42, 0
	v_smfmac_f32_16x16x64_f16 v[230:233], v[150:153], a[160:167], v210
	ds_write_b16 v207, v240
	v_smfmac_f32_16x16x64_f16 v[234:237], v[150:153], v[98:105], v210
	ds_write_b16 v207, v243 offset:544
	v_smfmac_f32_16x16x64_f16 v[230:233], v[154:157], a[192:199], v210
	ds_write_b16 v207, v241 offset:1088
	v_smfmac_f32_16x16x64_f16 v[234:237], v[154:157], v[106:113], v210
	ds_read_b128 v[238:241], v217
	v_smfmac_f32_16x16x64_f16 v[230:233], v[158:161], a[224:231], v210
	ds_read_b128 v[242:245], v217
	v_smfmac_f32_16x16x64_f16 v[234:237], v[158:161], v[122:129], v210
	s_waitcnt lgkmcnt(1)
	v_smfmac_f32_16x16x64_f16 v[238:241], v[130:133], a[8:15], v210
	s_waitcnt lgkmcnt(0)
	v_smfmac_f32_16x16x64_f16 v[242:245], v[130:133], v[2:9], v210
	v_smfmac_f32_16x16x64_f16 v[238:241], v[134:137], a[32:39], v210
	v_fmac_f32_e32 v230, s40, v231
	v_fmac_f32_e32 v234, s40, v235
	v_smfmac_f32_16x16x64_f16 v[242:245], v[134:137], v[10:17], v210
	v_fmac_f32_e32 v230, s41, v232
	v_fmac_f32_e32 v234, s41, v236
	v_smfmac_f32_16x16x64_f16 v[238:241], v[138:141], a[72:79], v210
	s_nop 0
	v_permlane32_swap_b32_e32 v230, v234
	v_add_f32_e32 v219, v230, v234
	v_smfmac_f32_16x16x64_f16 v[242:245], v[138:141], v[50:57], v210
	v_fmac_f32_e32 v248, 0xbe8c0c4c, v219
	v_fma_mixlo_f16 v232, v178, v248, v171
	v_smfmac_f32_16x16x64_f16 v[238:241], v[142:145], a[104:111], v210
	v_fma_f32 v231, v178, v248, v171
	v_fma_mix_f32 v231, v231, 1.0, -v232 op_sel_hi:[0,0,1]
	v_smfmac_f32_16x16x64_f16 v[242:245], v[142:145], v[26:33], v210
	v_fma_mixlo_f16 v235, v231, s42, 0
	v_smfmac_f32_16x16x64_f16 v[238:241], v[146:149], a[136:143], v210
	v_fma_mix_f32 v231, v231, s42, -v235 op_sel_hi:[0,0,1]
	v_smfmac_f32_16x16x64_f16 v[242:245], v[146:149], v[82:89], v210
	v_fma_mixlo_f16 v233, v231, s42, 0
	v_smfmac_f32_16x16x64_f16 v[238:241], v[150:153], a[168:175], v210
	ds_write_b16 v204, v232
	v_smfmac_f32_16x16x64_f16 v[242:245], v[150:153], v[66:73], v210
	ds_write_b16 v204, v235 offset:544
	v_smfmac_f32_16x16x64_f16 v[238:241], v[154:157], a[200:207], v210
	ds_write_b16 v204, v233 offset:1088
	v_smfmac_f32_16x16x64_f16 v[242:245], v[154:157], v[114:121], v210
	ds_read_b128 v[230:233], v217
	v_smfmac_f32_16x16x64_f16 v[238:241], v[158:161], a[232:239], v210
	ds_read_b128 v[234:237], v217
	v_smfmac_f32_16x16x64_f16 v[242:245], v[158:161], v[90:97], v210
	s_nop 5
	v_fmac_f32_e32 v238, s40, v239
	s_nop 0
	v_fmac_f32_e32 v242, s40, v243
	v_fmac_f32_e32 v238, s41, v240
	v_fmac_f32_e32 v242, s41, v244
	s_nop 1
	v_permlane32_swap_b32_e32 v238, v242
	v_add_f32_e32 v220, v238, v242
	v_fmac_f32_e32 v249, 0xbe8c0c4c, v220
	v_fma_mixlo_f16 v240, v178, v249, v170
	v_fma_f32 v239, v178, v249, v170
	v_fma_mix_f32 v239, v239, 1.0, -v240 op_sel_hi:[0,0,1]
	v_fma_mixlo_f16 v243, v239, s42, 0
	v_fma_mix_f32 v239, v239, s42, -v243 op_sel_hi:[0,0,1]
	v_fma_mixlo_f16 v241, v239, s42, 0
	ds_write_b16 v205, v240
	ds_write_b16 v205, v243 offset:544
	ds_write_b16 v205, v241 offset:1088
	ds_read_b128 v[180:183], v199 offset:0
	ds_read_b128 v[184:187], v199 offset:1024
	ds_read_b128 v[188:191], v199 offset:4096
	ds_read_b128 v[192:195], v199 offset:5120
	ds_read_b128 v[222:225], v199 offset:8192
	s_waitcnt lgkmcnt(6)
	ds_read_b128 v[226:229], v199 offset:9216
	s_waitcnt lgkmcnt(0)
	s_barrier
	ds_read_b128 v[130:133], v208
	ds_read_b128 v[134:137], v209 offset:64
	ds_read_b128 v[138:141], v211
	ds_read_b128 v[142:145], v212
	ds_read_b128 v[146:149], v213
	ds_read_b128 v[150:153], v214
	ds_read_b128 v[154:157], v215
	ds_read_b128 v[158:161], v216
	s_waitcnt lgkmcnt(7)
	v_smfmac_f32_16x16x64_f16 v[230:233], v[130:133], a[16:23], v210
	ds_read_b128 v[238:241], v217
	ds_read_b128 v[242:245], v217
	v_smfmac_f32_16x16x64_f16 v[234:237], v[130:133], v[180:187], v210
	ds_read_b128 v[180:183], v199 offset:12288
	ds_read_b128 v[184:187], v199 offset:13312
	v_mul_f32_e32 v252, 0x3dbaaaab, v173
	v_fmac_f32_e32 v252, 0x3ee6024d, v166
	s_waitcnt lgkmcnt(10)
	v_smfmac_f32_16x16x64_f16 v[230:233], v[134:137], a[48:55], v210
	v_fmac_f32_e32 v252, 0x3f26aaab, v179
	v_fmac_f32_e32 v252, 0xbea50e7e, v219
	v_smfmac_f32_16x16x64_f16 v[234:237], v[134:137], v[188:195], v210
	ds_read_b128 v[188:191], v199 offset:16384
	ds_read_b128 v[192:195], v199 offset:17408
	v_mul_f32_e32 v253, 0x3dbaaaab, v172
	s_waitcnt lgkmcnt(11)
	v_smfmac_f32_16x16x64_f16 v[230:233], v[138:141], a[80:87], v210
	v_fmac_f32_e32 v253, 0x3ee6024d, v167
	v_smfmac_f32_16x16x64_f16 v[234:237], v[138:141], v[222:229], v210
	ds_read_b128 v[222:225], v199 offset:20480
	ds_read_b128 v[226:229], v199 offset:21504
	v_fmac_f32_e32 v253, 0x3f26aaab, v196
	s_waitcnt lgkmcnt(12)
	v_smfmac_f32_16x16x64_f16 v[230:233], v[142:145], a[112:119], v210
	v_fmac_f32_e32 v253, 0xbea50e7e, v220
	s_waitcnt lgkmcnt(4)
	v_smfmac_f32_16x16x64_f16 v[234:237], v[142:145], v[180:187], v210
	ds_read_b128 v[180:183], v199 offset:24576
	ds_read_b128 v[184:187], v199 offset:25600
	v_mul_f32_e32 v254, 0x3dbaaaab, v175
	v_smfmac_f32_16x16x64_f16 v[230:233], v[146:149], a[144:151], v210
	v_fmac_f32_e32 v254, 0x3ee6024d, v176
	s_waitcnt lgkmcnt(4)
	v_smfmac_f32_16x16x64_f16 v[234:237], v[146:149], v[188:195], v210
	ds_read_b128 v[188:191], v199 offset:28672
	ds_read_b128 v[192:195], v199 offset:29696
	v_fmac_f32_e32 v254, 0x3f26aaab, v197
	v_smfmac_f32_16x16x64_f16 v[230:233], v[150:153], a[176:183], v210
	v_fmac_f32_e32 v254, 0xbea50e7e, v246
	s_waitcnt lgkmcnt(4)
	v_smfmac_f32_16x16x64_f16 v[234:237], v[150:153], v[222:229], v210
	ds_read_b128 v[222:225], v199 offset:2048
	ds_read_b128 v[226:229], v199 offset:3072
	v_mul_f32_e32 v255, 0x3dbaaaab, v174
	v_smfmac_f32_16x16x64_f16 v[230:233], v[154:157], a[208:215], v210
	v_fmac_f32_e32 v255, 0x3ee6024d, v177
	s_waitcnt lgkmcnt(4)
	v_smfmac_f32_16x16x64_f16 v[234:237], v[154:157], v[180:187], v210
	ds_read_b128 v[180:183], v199 offset:6144
	ds_read_b128 v[184:187], v199 offset:7168
	v_fmac_f32_e32 v255, 0x3f26aaab, v198
	v_smfmac_f32_16x16x64_f16 v[230:233], v[158:161], a[240:247], v210
	v_fmac_f32_e32 v255, 0xbea50e7e, v247
	s_waitcnt lgkmcnt(4)
	v_smfmac_f32_16x16x64_f16 v[234:237], v[158:161], v[188:195], v210
	ds_read_b128 v[188:191], v199 offset:10240
	ds_read_b128 v[192:195], v199 offset:11264
	v_smfmac_f32_16x16x64_f16 v[238:241], v[130:133], a[24:31], v210
	s_waitcnt lgkmcnt(4)
	v_smfmac_f32_16x16x64_f16 v[242:245], v[130:133], v[222:229], v210
	ds_read_b128 v[222:225], v199 offset:14336
	ds_read_b128 v[226:229], v199 offset:15360
	v_smfmac_f32_16x16x64_f16 v[238:241], v[134:137], a[56:63], v210
	v_fmac_f32_e32 v230, s40, v231
	v_fmac_f32_e32 v234, s40, v235
	s_waitcnt lgkmcnt(4)
	v_smfmac_f32_16x16x64_f16 v[242:245], v[134:137], v[180:187], v210
	ds_read_b128 v[180:183], v199 offset:18432
	ds_read_b128 v[184:187], v199 offset:19456
	v_fmac_f32_e32 v230, s41, v232
	v_fmac_f32_e32 v234, s41, v236
	v_smfmac_f32_16x16x64_f16 v[238:241], v[138:141], a[88:95], v210
	s_nop 0
	v_permlane32_swap_b32_e32 v230, v234
	v_add_f32_e32 v250, v230, v234
	s_waitcnt lgkmcnt(4)
	v_smfmac_f32_16x16x64_f16 v[242:245], v[138:141], v[188:195], v210
	ds_read_b128 v[188:191], v199 offset:22528
	ds_read_b128 v[192:195], v199 offset:23552
	v_fmac_f32_e32 v254, 0x3e061862, v250
	v_mov_b32_e32 v236, v254
	v_smfmac_f32_16x16x64_f16 v[238:241], v[142:145], a[120:127], v210
	v_fma_mixlo_f16 v232, v178, v236, v169
	v_fma_f32 v254, v178, v236, v169
	s_waitcnt lgkmcnt(4)
	v_smfmac_f32_16x16x64_f16 v[242:245], v[142:145], v[222:229], v210
	ds_read_b128 v[222:225], v199 offset:26624
	ds_read_b128 v[226:229], v199 offset:27648
	v_fma_mix_f32 v231, v254, 1.0, -v232 op_sel_hi:[0,0,1]
	v_fma_mixlo_f16 v235, v231, s42, 0
	v_smfmac_f32_16x16x64_f16 v[238:241], v[146:149], a[152:159], v210
	v_fma_mix_f32 v231, v231, s42, -v235 op_sel_hi:[0,0,1]
	s_waitcnt lgkmcnt(4)
	v_smfmac_f32_16x16x64_f16 v[242:245], v[146:149], v[180:187], v210
	ds_read_b128 v[180:183], v199 offset:30720
	ds_read_b128 v[184:187], v199 offset:31744
	v_fma_mixlo_f16 v233, v231, s42, 0
	v_smfmac_f32_16x16x64_f16 v[238:241], v[150:153], a[184:191], v210
	ds_write_b16 v206, v232 offset:8704
	s_waitcnt lgkmcnt(5)
	v_smfmac_f32_16x16x64_f16 v[242:245], v[150:153], v[188:195], v210
	ds_write_b16 v206, v235 offset:9248
	v_smfmac_f32_16x16x64_f16 v[238:241], v[154:157], a[216:223], v210
	ds_write_b16 v206, v233 offset:9792
	s_waitcnt lgkmcnt(5)
	v_smfmac_f32_16x16x64_f16 v[242:245], v[154:157], v[222:229], v210
	ds_read_b128 v[230:233], v217
	v_smfmac_f32_16x16x64_f16 v[238:241], v[158:161], a[248:255], v210
	ds_read_b128 v[234:237], v217
	s_waitcnt lgkmcnt(5)
	v_smfmac_f32_16x16x64_f16 v[242:245], v[158:161], v[180:187], v210
	s_waitcnt lgkmcnt(1)
	v_smfmac_f32_16x16x64_f16 v[230:233], v[130:133], a[0:7], v210
	s_waitcnt lgkmcnt(0)
	v_smfmac_f32_16x16x64_f16 v[234:237], v[130:133], v[18:25], v210
	v_smfmac_f32_16x16x64_f16 v[230:233], v[134:137], a[40:47], v210
	v_fmac_f32_e32 v238, s40, v239
	v_fmac_f32_e32 v242, s40, v243
	v_smfmac_f32_16x16x64_f16 v[234:237], v[134:137], v[34:41], v210
	v_fmac_f32_e32 v238, s41, v240
	v_fmac_f32_e32 v242, s41, v244
	v_smfmac_f32_16x16x64_f16 v[230:233], v[138:141], a[64:71], v210
	s_nop 0
	v_permlane32_swap_b32_e32 v238, v242
	v_add_f32_e32 v251, v238, v242
	v_smfmac_f32_16x16x64_f16 v[234:237], v[138:141], v[42:49], v210
	v_fmac_f32_e32 v255, 0x3e061862, v251
	v_mov_b32_e32 v244, v255
	v_smfmac_f32_16x16x64_f16 v[230:233], v[142:145], a[96:103], v210
	v_fma_mixlo_f16 v240, v178, v244, v168
	v_fma_f32 v255, v178, v244, v168
	v_smfmac_f32_16x16x64_f16 v[234:237], v[142:145], v[58:65], v210
	v_fma_mix_f32 v239, v255, 1.0, -v240 op_sel_hi:[0,0,1]
	v_fma_mixlo_f16 v243, v239, s42, 0
	v_smfmac_f32_16x16x64_f16 v[230:233], v[146:149], a[128:135], v210
	v_fma_mix_f32 v239, v239, s42, -v243 op_sel_hi:[0,0,1]
	v_smfmac_f32_16x16x64_f16 v[234:237], v[146:149], v[74:81], v210
	v_fma_mixlo_f16 v241, v239, s42, 0
	v_smfmac_f32_16x16x64_f16 v[230:233], v[150:153], a[160:167], v210
	ds_write_b16 v207, v240 offset:8704
	v_smfmac_f32_16x16x64_f16 v[234:237], v[150:153], v[98:105], v210
	ds_write_b16 v207, v243 offset:9248
	v_smfmac_f32_16x16x64_f16 v[230:233], v[154:157], a[192:199], v210
	ds_write_b16 v207, v241 offset:9792
	v_smfmac_f32_16x16x64_f16 v[234:237], v[154:157], v[106:113], v210
	ds_read_b128 v[238:241], v217
	v_smfmac_f32_16x16x64_f16 v[230:233], v[158:161], a[224:231], v210
	ds_read_b128 v[242:245], v217
	v_smfmac_f32_16x16x64_f16 v[234:237], v[158:161], v[122:129], v210
	s_waitcnt lgkmcnt(1)
	v_smfmac_f32_16x16x64_f16 v[238:241], v[130:133], a[8:15], v210
	s_waitcnt lgkmcnt(0)
	v_smfmac_f32_16x16x64_f16 v[242:245], v[130:133], v[2:9], v210
	v_smfmac_f32_16x16x64_f16 v[238:241], v[134:137], a[32:39], v210
	v_fmac_f32_e32 v230, s40, v231
	v_fmac_f32_e32 v234, s40, v235
	v_smfmac_f32_16x16x64_f16 v[242:245], v[134:137], v[10:17], v210
	v_fmac_f32_e32 v230, s41, v232
	v_fmac_f32_e32 v234, s41, v236
	v_smfmac_f32_16x16x64_f16 v[238:241], v[138:141], a[72:79], v210
	s_nop 0
	v_permlane32_swap_b32_e32 v230, v234
	v_add_f32_e32 v248, v230, v234
	v_smfmac_f32_16x16x64_f16 v[242:245], v[138:141], v[50:57], v210
	v_fmac_f32_e32 v252, 0x3e061862, v248
	v_mov_b32_e32 v236, v252
	v_smfmac_f32_16x16x64_f16 v[238:241], v[142:145], a[104:111], v210
	v_fma_mixlo_f16 v232, v178, v236, v171
	v_fma_f32 v252, v178, v236, v171
	v_smfmac_f32_16x16x64_f16 v[242:245], v[142:145], v[26:33], v210
	v_fma_mix_f32 v231, v252, 1.0, -v232 op_sel_hi:[0,0,1]
	v_fma_mixlo_f16 v235, v231, s42, 0
	v_smfmac_f32_16x16x64_f16 v[238:241], v[146:149], a[136:143], v210
	v_fma_mix_f32 v231, v231, s42, -v235 op_sel_hi:[0,0,1]
	v_smfmac_f32_16x16x64_f16 v[242:245], v[146:149], v[82:89], v210
	v_fma_mixlo_f16 v233, v231, s42, 0
	v_smfmac_f32_16x16x64_f16 v[238:241], v[150:153], a[168:175], v210
	ds_write_b16 v204, v232 offset:8704
	v_smfmac_f32_16x16x64_f16 v[242:245], v[150:153], v[66:73], v210
	ds_write_b16 v204, v235 offset:9248
	v_smfmac_f32_16x16x64_f16 v[238:241], v[154:157], a[200:207], v210
	ds_write_b16 v204, v233 offset:9792
	v_smfmac_f32_16x16x64_f16 v[242:245], v[154:157], v[114:121], v210
	ds_read_b128 v[230:233], v217
	v_smfmac_f32_16x16x64_f16 v[238:241], v[158:161], a[232:239], v210
	ds_read_b128 v[234:237], v217
	v_smfmac_f32_16x16x64_f16 v[242:245], v[158:161], v[90:97], v210
	s_nop 5
	v_fmac_f32_e32 v238, s40, v239
	s_nop 0
	v_fmac_f32_e32 v242, s40, v243
	v_fmac_f32_e32 v238, s41, v240
	v_fmac_f32_e32 v242, s41, v244
	s_nop 1
	v_permlane32_swap_b32_e32 v238, v242
	v_add_f32_e32 v249, v238, v242
	v_fmac_f32_e32 v253, 0x3e061862, v249
	v_mov_b32_e32 v244, v253
	v_fma_mixlo_f16 v240, v178, v244, v170
	v_fma_f32 v253, v178, v244, v170
	v_fma_mix_f32 v239, v253, 1.0, -v240 op_sel_hi:[0,0,1]
	v_fma_mixlo_f16 v243, v239, s42, 0
	v_fma_mix_f32 v239, v239, s42, -v243 op_sel_hi:[0,0,1]
	v_fma_mixlo_f16 v241, v239, s42, 0
	ds_write_b16 v205, v240 offset:8704
	ds_write_b16 v205, v243 offset:9248
	ds_write_b16 v205, v241 offset:9792
	ds_read_b128 v[180:183], v199 offset:0
	ds_read_b128 v[184:187], v199 offset:1024
	ds_read_b128 v[188:191], v199 offset:4096
	ds_read_b128 v[192:195], v199 offset:5120
	ds_read_b128 v[222:225], v199 offset:8192
	s_waitcnt lgkmcnt(6)
	ds_read_b128 v[226:229], v199 offset:9216
	s_waitcnt lgkmcnt(0)
	s_barrier
	ds_read_b128 v[130:133], v208 offset:8704
	ds_read_b128 v[134:137], v209 offset:8768
	ds_read_b128 v[138:141], v211 offset:8704
	ds_read_b128 v[142:145], v212 offset:8704
	ds_read_b128 v[146:149], v213 offset:8704
	ds_read_b128 v[150:153], v214 offset:8704
	ds_read_b128 v[154:157], v215 offset:8704
	ds_read_b128 v[158:161], v216 offset:8704
	s_waitcnt lgkmcnt(7)
	v_smfmac_f32_16x16x64_f16 v[230:233], v[130:133], a[16:23], v210
	ds_read_b128 v[238:241], v217
	ds_read_b128 v[242:245], v217
	v_smfmac_f32_16x16x64_f16 v[234:237], v[130:133], v[180:187], v210
	ds_read_b128 v[180:183], v199 offset:12288
	ds_read_b128 v[184:187], v199 offset:13312
	v_mul_f32_e32 v162, 0x3aa1907f, v173
	v_fmac_f32_e32 v162, 0xbb8b5ad3, v166
	s_waitcnt lgkmcnt(10)
	v_smfmac_f32_16x16x64_f16 v[230:233], v[134:137], a[48:55], v210
	v_fmac_f32_e32 v162, 0x3d177777, v179
	v_fmac_f32_e32 v162, 0xbd50568f, v219
	v_smfmac_f32_16x16x64_f16 v[234:237], v[134:137], v[188:195], v210
	ds_read_b128 v[188:191], v199 offset:16384
	ds_read_b128 v[192:195], v199 offset:17408
	v_fmac_f32_e32 v162, 0x3d2ba454, v248
	v_mul_f32_e32 v163, 0x3aa1907f, v172
	s_waitcnt lgkmcnt(11)
	v_smfmac_f32_16x16x64_f16 v[230:233], v[138:141], a[80:87], v210
	v_fmac_f32_e32 v163, 0xbb8b5ad3, v167
	v_fmac_f32_e32 v163, 0x3d177777, v196
	v_smfmac_f32_16x16x64_f16 v[234:237], v[138:141], v[222:229], v210
	ds_read_b128 v[222:225], v199 offset:20480
	ds_read_b128 v[226:229], v199 offset:21504
	v_fmac_f32_e32 v163, 0xbd50568f, v220
	v_fmac_f32_e32 v163, 0x3d2ba454, v249
	s_waitcnt lgkmcnt(12)
	v_smfmac_f32_16x16x64_f16 v[230:233], v[142:145], a[112:119], v210
	v_mul_f32_e32 v164, 0x3aa1907f, v175
	v_fmac_f32_e32 v164, 0xbb8b5ad3, v176
	s_waitcnt lgkmcnt(4)
	v_smfmac_f32_16x16x64_f16 v[234:237], v[142:145], v[180:187], v210
	ds_read_b128 v[180:183], v199 offset:24576
	ds_read_b128 v[184:187], v199 offset:25600
	v_fmac_f32_e32 v164, 0x3d177777, v197
	v_fmac_f32_e32 v164, 0xbd50568f, v246
	v_smfmac_f32_16x16x64_f16 v[230:233], v[146:149], a[144:151], v210
	v_fmac_f32_e32 v164, 0x3d2ba454, v250
	v_mul_f32_e32 v165, 0x3aa1907f, v174
	s_waitcnt lgkmcnt(4)
	v_smfmac_f32_16x16x64_f16 v[234:237], v[146:149], v[188:195], v210
	ds_read_b128 v[188:191], v199 offset:28672
	ds_read_b128 v[192:195], v199 offset:29696
	v_fmac_f32_e32 v165, 0xbb8b5ad3, v177
	v_fmac_f32_e32 v165, 0x3d177777, v198
	v_smfmac_f32_16x16x64_f16 v[230:233], v[150:153], a[176:183], v210
	v_fmac_f32_e32 v165, 0xbd50568f, v247
	v_fmac_f32_e32 v165, 0x3d2ba454, v251
	s_waitcnt lgkmcnt(4)
	v_smfmac_f32_16x16x64_f16 v[234:237], v[150:153], v[222:229], v210
	ds_read_b128 v[222:225], v199 offset:2048
	ds_read_b128 v[226:229], v199 offset:3072
	v_max_f32_e64 v179, |v171|, |v252|
	v_mov_b32_e32 v248, 0x358637bd
	v_smfmac_f32_16x16x64_f16 v[230:233], v[154:157], a[208:215], v210
	v_fmac_f32_e32 v248, 0x3a83126f, v179
	v_rcp_f32_e32 v179, v248
	s_waitcnt lgkmcnt(4)
	v_smfmac_f32_16x16x64_f16 v[234:237], v[154:157], v[180:187], v210
	ds_read_b128 v[180:183], v199 offset:6144
	ds_read_b128 v[184:187], v199 offset:7168
	v_max_f32_e64 v196, |v170|, |v253|
	v_mov_b32_e32 v249, 0x358637bd
	v_smfmac_f32_16x16x64_f16 v[230:233], v[158:161], a[240:247], v210
	v_fmac_f32_e32 v249, 0x3a83126f, v196
	v_rcp_f32_e32 v196, v249
	s_waitcnt lgkmcnt(4)
	v_smfmac_f32_16x16x64_f16 v[234:237], v[158:161], v[188:195], v210
	ds_read_b128 v[188:191], v199 offset:10240
	ds_read_b128 v[192:195], v199 offset:11264
	v_max_f32_e64 v197, |v169|, |v254|
	v_mov_b32_e32 v250, 0x358637bd
	v_fmac_f32_e32 v250, 0x3a83126f, v197
	v_rcp_f32_e32 v197, v250
	v_max_f32_e64 v198, |v168|, |v255|
	v_mov_b32_e32 v251, 0x358637bd
	v_fmac_f32_e32 v251, 0x3a83126f, v198
	v_rcp_f32_e32 v198, v251
	v_smfmac_f32_16x16x64_f16 v[238:241], v[130:133], a[24:31], v210
	s_waitcnt lgkmcnt(4)
	v_smfmac_f32_16x16x64_f16 v[242:245], v[130:133], v[222:229], v210
	ds_read_b128 v[222:225], v199 offset:14336
	ds_read_b128 v[226:229], v199 offset:15360
	v_smfmac_f32_16x16x64_f16 v[238:241], v[134:137], a[56:63], v210
	v_fmac_f32_e32 v230, s40, v231
	s_waitcnt lgkmcnt(4)
	v_smfmac_f32_16x16x64_f16 v[242:245], v[134:137], v[180:187], v210
	ds_read_b128 v[180:183], v199 offset:18432
	ds_read_b128 v[184:187], v199 offset:19456
	v_fmac_f32_e32 v234, s40, v235
	v_smfmac_f32_16x16x64_f16 v[238:241], v[138:141], a[88:95], v210
	v_fmac_f32_e32 v230, s41, v232
	s_waitcnt lgkmcnt(4)
	v_smfmac_f32_16x16x64_f16 v[242:245], v[138:141], v[188:195], v210
	ds_read_b128 v[188:191], v199 offset:22528
	ds_read_b128 v[192:195], v199 offset:23552
	v_fmac_f32_e32 v234, s41, v236
	v_smfmac_f32_16x16x64_f16 v[238:241], v[142:145], a[120:127], v210
	s_nop 0
	v_permlane32_swap_b32_e32 v230, v234
	s_waitcnt lgkmcnt(4)
	v_smfmac_f32_16x16x64_f16 v[242:245], v[142:145], v[222:229], v210
	ds_read_b128 v[222:225], v199 offset:26624
	ds_read_b128 v[226:229], v199 offset:27648
	v_add_f32_e32 v176, v230, v234
	v_smfmac_f32_16x16x64_f16 v[238:241], v[146:149], a[152:159], v210
	v_fmac_f32_e32 v164, 0xbccccccd, v176
	s_waitcnt lgkmcnt(4)
	v_smfmac_f32_16x16x64_f16 v[242:245], v[146:149], v[180:187], v210
	ds_read_b128 v[180:183], v199 offset:30720
	ds_read_b128 v[184:187], v199 offset:31744
	v_mul_f32_e32 v231, v178, v164
	v_smfmac_f32_16x16x64_f16 v[238:241], v[150:153], a[184:191], v210
	v_mul_f32_e32 v231, v231, v197
	s_waitcnt lgkmcnt(4)
	v_smfmac_f32_16x16x64_f16 v[242:245], v[150:153], v[188:195], v210
	v_mul_f32_e32 v219, v231, v231
	v_smfmac_f32_16x16x64_f16 v[238:241], v[154:157], a[216:223], v210
	ds_read_b128 v[230:233], v217
	s_waitcnt lgkmcnt(3)
	v_smfmac_f32_16x16x64_f16 v[242:245], v[154:157], v[222:229], v210
	ds_read_b128 v[234:237], v217
	v_smfmac_f32_16x16x64_f16 v[238:241], v[158:161], a[248:255], v210
	s_waitcnt lgkmcnt(2)
	v_smfmac_f32_16x16x64_f16 v[242:245], v[158:161], v[180:187], v210
	s_waitcnt lgkmcnt(1)
	v_smfmac_f32_16x16x64_f16 v[230:233], v[130:133], a[0:7], v210
	s_waitcnt lgkmcnt(0)
	v_smfmac_f32_16x16x64_f16 v[234:237], v[130:133], v[18:25], v210
	v_smfmac_f32_16x16x64_f16 v[230:233], v[134:137], a[40:47], v210
	v_fmac_f32_e32 v238, s40, v239
	v_smfmac_f32_16x16x64_f16 v[234:237], v[134:137], v[34:41], v210
	v_fmac_f32_e32 v242, s40, v243
	v_smfmac_f32_16x16x64_f16 v[230:233], v[138:141], a[64:71], v210
	v_fmac_f32_e32 v238, s41, v240
	v_smfmac_f32_16x16x64_f16 v[234:237], v[138:141], v[42:49], v210
	v_fmac_f32_e32 v242, s41, v244
	v_smfmac_f32_16x16x64_f16 v[230:233], v[142:145], a[96:103], v210
	s_nop 0
	v_permlane32_swap_b32_e32 v238, v242
	v_smfmac_f32_16x16x64_f16 v[234:237], v[142:145], v[58:65], v210
	v_add_f32_e32 v177, v238, v242
	v_smfmac_f32_16x16x64_f16 v[230:233], v[146:149], a[128:135], v210
	v_fmac_f32_e32 v165, 0xbccccccd, v177
	v_smfmac_f32_16x16x64_f16 v[234:237], v[146:149], v[74:81], v210
	v_mul_f32_e32 v239, v178, v165
	v_smfmac_f32_16x16x64_f16 v[230:233], v[150:153], a[160:167], v210
	v_mul_f32_e32 v239, v239, v198
	v_smfmac_f32_16x16x64_f16 v[234:237], v[150:153], v[98:105], v210
	v_fmac_f32_e32 v219, v239, v239
	v_smfmac_f32_16x16x64_f16 v[230:233], v[154:157], a[192:199], v210
	ds_read_b128 v[238:241], v217
	v_smfmac_f32_16x16x64_f16 v[234:237], v[154:157], v[106:113], v210
	ds_read_b128 v[242:245], v217
	v_smfmac_f32_16x16x64_f16 v[230:233], v[158:161], a[224:231], v210
	v_smfmac_f32_16x16x64_f16 v[234:237], v[158:161], v[122:129], v210
	s_waitcnt lgkmcnt(1)
	v_smfmac_f32_16x16x64_f16 v[238:241], v[130:133], a[8:15], v210
	s_waitcnt lgkmcnt(0)
	v_smfmac_f32_16x16x64_f16 v[242:245], v[130:133], v[2:9], v210
	v_smfmac_f32_16x16x64_f16 v[238:241], v[134:137], a[32:39], v210
	v_fmac_f32_e32 v230, s40, v231
	v_smfmac_f32_16x16x64_f16 v[242:245], v[134:137], v[10:17], v210
	v_fmac_f32_e32 v234, s40, v235
	v_smfmac_f32_16x16x64_f16 v[238:241], v[138:141], a[72:79], v210
	v_fmac_f32_e32 v230, s41, v232
	v_smfmac_f32_16x16x64_f16 v[242:245], v[138:141], v[50:57], v210
	v_fmac_f32_e32 v234, s41, v236
	v_smfmac_f32_16x16x64_f16 v[238:241], v[142:145], a[104:111], v210
	s_nop 0
	v_permlane32_swap_b32_e32 v230, v234
	v_smfmac_f32_16x16x64_f16 v[242:245], v[142:145], v[26:33], v210
	v_add_f32_e32 v166, v230, v234
	v_smfmac_f32_16x16x64_f16 v[238:241], v[146:149], a[136:143], v210
	v_fmac_f32_e32 v162, 0xbccccccd, v166
	v_smfmac_f32_16x16x64_f16 v[242:245], v[146:149], v[82:89], v210
	v_mul_f32_e32 v231, v178, v162
	v_smfmac_f32_16x16x64_f16 v[238:241], v[150:153], a[168:175], v210
	v_mul_f32_e32 v231, v231, v179
	v_smfmac_f32_16x16x64_f16 v[242:245], v[150:153], v[66:73], v210
	v_fmac_f32_e32 v219, v231, v231
	v_smfmac_f32_16x16x64_f16 v[238:241], v[154:157], a[200:207], v210
	ds_read_b128 v[230:233], v217
	v_smfmac_f32_16x16x64_f16 v[242:245], v[154:157], v[114:121], v210
	ds_read_b128 v[234:237], v217
	v_smfmac_f32_16x16x64_f16 v[238:241], v[158:161], a[232:239], v210
	v_smfmac_f32_16x16x64_f16 v[242:245], v[158:161], v[90:97], v210
	s_nop 6
	v_fmac_f32_e32 v238, s40, v239
	v_fmac_f32_e32 v242, s40, v243
	v_fmac_f32_e32 v238, s41, v240
	v_fmac_f32_e32 v242, s41, v244
	s_nop 1
	v_permlane32_swap_b32_e32 v238, v242
	v_add_f32_e32 v167, v238, v242
	v_fmac_f32_e32 v163, 0xbccccccd, v167
	v_mul_f32_e32 v239, v178, v163
	v_mul_f32_e32 v239, v239, v196
	v_fmac_f32_e32 v219, v239, v239
	ds_read_b128 v[180:183], v199 offset:0
	ds_read_b128 v[184:187], v199 offset:1024
	ds_read_b128 v[188:191], v199 offset:4096
	ds_read_b128 v[192:195], v199 offset:5120
	ds_read_b128 v[222:225], v199 offset:8192
	ds_read_b128 v[226:229], v199 offset:9216
	v_add_f32_dpp v238, v219, v219 quad_perm:[1,0,3,2] row_mask:0xf bank_mask:0xf bound_ctrl:1
	s_nop 1
	v_add_f32_dpp v238, v238, v238 quad_perm:[2,3,0,1] row_mask:0xf bank_mask:0xf bound_ctrl:1
	s_nop 1
	v_add_f32_dpp v238, v238, v238 row_half_mirror row_mask:0xf bank_mask:0xf bound_ctrl:1
	s_nop 1
	v_add_f32_dpp v238, v238, v238 row_mirror row_mask:0xf bank_mask:0xf bound_ctrl:1
	v_mov_b32_e32 v239, v238
	s_nop 1
	v_permlane32_swap_b32_e32 v238, v239
	v_add_f32_e32 v238, v238, v239
	v_lshl_add_u32 v240, s29, 6, v218
	v_lshlrev_b32_e32 v241, 3, v201
	v_or_b32_e32 v241, 0x24400, v241
	v_lshl_add_u32 v241, s29, 6, v241
	s_and_saveexec_b64 s[2:3], s[4:5]
	ds_write_b32 v240, v238
	s_or_b64 exec, exec, s[2:3]
	s_waitcnt lgkmcnt(0)
	s_barrier
	ds_read2_b32 v[130:131], v241 offset1:4
	ds_read2_b32 v[132:133], v241 offset0:8 offset1:12
	s_waitcnt lgkmcnt(1)
	v_add_f32_e32 v238, v130, v131
	s_waitcnt lgkmcnt(0)
	v_add_f32_e32 v238, v238, v132
	v_add_f32_e32 v238, v238, v133
	v_mul_f32_e32 v238, 0x3b000000, v238
	v_max_f32_e32 v238, 0xda24260, v238
	v_sqrt_f32_e32 v238, v238
	s_nop 0
	v_cmp_ngt_f32_e64 s[2:3], 1.0, v238
	v_cmp_gt_f32_e32 vcc, 1.0, v238
	v_log_f32_e32 v239, v238
	v_mul_f32_e32 v241, 0x44000000, v178
	s_and_saveexec_b64 s[26:27], vcc
	v_add_f32_e32 v221, v221, v241
	v_mov_b32_e32 v171, v252
	v_mov_b32_e32 v173, v166
	v_mov_b32_e32 v170, v253
	v_mov_b32_e32 v172, v167
	v_mov_b32_e32 v169, v254
	v_mov_b32_e32 v175, v176
	v_mov_b32_e32 v168, v255
	v_mov_b32_e32 v174, v177
	s_or_b64 exec, exec, s[26:27]
	v_mov_b32_e32 v240, 0x41200000
	s_nop 0
	v_cndmask_b32_e64 v240, v240, 1.0, s[22:23]
	s_xor_b32 s29, s29, 1
	s_add_i32 s30, s30, 1
	v_mul_f32_e32 v239, 0xbe4ccccd, v239
	v_exp_f32_e32 v239, v239
	s_nop 0
	v_mul_f32_e32 v239, 0x3f666666, v239
	v_min_f32_e32 v240, v239, v240
	v_max_f32_e32 v239, 0x3e4ccccd, v239
	v_cndmask_b32_e64 v239, v240, v239, s[2:3]
	v_mul_f32_e32 v1, v241, v239
	s_mov_b64 s[22:23], s[2:3]
	s_branch .Lrk_top
